# GEMM K-loops: scalar/address instructions opening each load segment moved in front of the preceding MMA-closing barrier
# baseline (speedup 1.0000x reference)
; #define PG8_STAGE(bufoff, gbase, voff) do { _Pragma("unroll") for (int _i = 0; _i < 2; ++_i) \
;         __builtin_amdgcn_global_load_lds((const unsigned*)((const char*)(gbase) + (voff)[_i]), (LAS unsigned*)(lds + (bufoff) + ldsw + _i * 8192), 16, 0, 0); } while (0)
; #define PG8_LDA(dst, b, h) do { _Pragma("unroll") for (int m = 0; m < 4; ++m) dst[m] = PG8_LD32(lds + PG8_SA(b, h) + aoff + m * 2048); } while (0)
; #define PG8_LDB(dst, b, h) do { _Pragma("unroll") for (int n = 0; n < 2; ++n) dst[n] = PG8_LD32(lds + PG8_SB(b, h) + boff + n * 2048); } while (0)
; #define PG8_WAIT_V(n) asm volatile("s_waitcnt vmcnt(" #n ")" ::: "memory")
; #define PG8_WAIT_L(n) asm volatile("s_waitcnt lgkmcnt(" #n ")" ::: "memory")
; #define PG8_BAR __builtin_amdgcn_s_barrier()
; #define PG8_SCHED __builtin_amdgcn_sched_barrier(0)
; #define PG8_STA(bufoff, nextflag, h, koff) do { if constexpr (Sched::GATHER) { unsigned _o[2]; _o[0] = (nextflag) ? nxtA[h][0] : curA[h][0]; _o[1] = (nextflag) ? nxtA[h][1] : curA[h][1]; PG8_STAGE(bufoff, Ab + (koff), _o); } \
;         else { PG8_STAGE(bufoff, ((nextflag) ? nA : cA) + (size_t)(h) * hstep + (koff), voffA); } } while (0)
; template <class Epi, class Sched, bool ALIGN_EPI, int DT>
; __device__ __forceinline__ void gemm_phase(LAS unsigned char* lds, const int KB, const Sched& S, const Epi& E) {
;     ...
;             const size_t k1 = (size_t)(t + 1) * kstep, k2 = last ? 0 : (size_t)(t + 2) * kstep, k3 = k2 + kstep;
;             const char* b2 = last ? nB : cB + (size_t)(t + 2) * kstep; const char* b3 = b2 + kstep;
;             PG8_LDB(B0, 0, 0); PG8_LDB(B1, 0, 1); PG8_SCHED; PG8_LDA(At, 0, 0); PG8_STA(PG8_SA(1, 1), false, 1, k1);
;             PG8_WAIT_V(8); PG8_WAIT_L(0); PG8_BAR; PG8_MMA(0, 0, At, B0); PG8_MMA(0, 1, At, B1); PG8_BAR; PG8_SCHED;
;             PG8_LDA(At, 0, 1); PG8_STAGE(PG8_SB(0, 0), b2, voffB); PG8_STAGE(PG8_SB(0, 1), b2 + hstep, voffB); PG8_STA(PG8_SA(0, 0), last, 0, k2);
;             PG8_WAIT_V(8); PG8_WAIT_L(0); PG8_BAR; PG8_MMA(1, 0, At, B0); PG8_MMA(1, 1, At, B1); PG8_BAR; PG8_SCHED;
.LBB0_193:
	ds_read_b128 v[152:155], v175
	ds_read_b128 v[156:159], v175 offset:1024
	ds_read_b128 v[160:163], v175 offset:2048
	ds_read_b128 v[164:167], v175 offset:3072
	ds_read_b128 v[168:171], v176
	ds_read_b128 v[182:185], v176 offset:1024
	ds_read_b128 v[186:189], v176 offset:2048
	ds_read_b128 v[190:193], v176 offset:3072
	s_add_u32 s38, s36, 0x100
	s_addc_u32 s39, s37, 0
	s_add_u32 s68, s25, s36
	s_addc_u32 s69, s66, s37
	s_cmp_eq_u32 s67, 12
	s_cselect_b64 s[42:43], -1, 0
	s_and_b64 s[40:41], s[42:43], exec
	s_cselect_b32 s70, 0, s38
	s_cselect_b32 s41, s0, s69
	s_cselect_b32 s40, s23, s68
	v_lshl_add_u64 v[228:229], v[148:149], 0, s[36:37]
	s_add_i32 m0, s45, 0xc000
	ds_read_b128 v[196:199], v177
	ds_read_b128 v[200:203], v177 offset:1024
	ds_read_b128 v[204:207], v177 offset:2048
	ds_read_b128 v[208:211], v177 offset:3072
	ds_read_b128 v[212:215], v177 offset:4096
	ds_read_b128 v[216:219], v177 offset:5120
	ds_read_b128 v[220:223], v177 offset:6144
	ds_read_b128 v[224:227], v177 offset:7168
	global_load_lds_dwordx4 v[228:229], off
	v_lshl_add_u64 v[228:229], v[150:151], 0, s[36:37]
	s_add_i32 m0, s45, 0xe000
	s_nop 0
	global_load_lds_dwordx4 v[228:229], off
	s_waitcnt vmcnt(8)
	s_waitcnt lgkmcnt(0)
	s_barrier
	s_setprio 1
	s_waitcnt lgkmcnt(0)
	v_mfma_i32_16x16x64_i8 v[126:129], v[152:155], v[196:199], v[126:129]
	v_mfma_i32_16x16x64_i8 v[122:125], v[160:163], v[196:199], v[122:125]
	v_mfma_i32_16x16x64_i8 v[110:113], v[152:155], v[204:207], v[110:113]
	v_mfma_i32_16x16x64_i8 v[106:109], v[160:163], v[204:207], v[106:109]
	v_mfma_i32_16x16x64_i8 v[94:97], v[152:155], v[212:215], v[94:97]
	v_mfma_i32_16x16x64_i8 v[90:93], v[160:163], v[212:215], v[90:93]
	v_mfma_i32_16x16x64_i8 v[78:81], v[152:155], v[220:223], v[78:81]
	v_mfma_i32_16x16x64_i8 v[74:77], v[160:163], v[220:223], v[74:77]
	v_mfma_i32_16x16x64_i8 v[126:129], v[156:159], v[200:203], v[126:129]
	v_mfma_i32_16x16x64_i8 v[122:125], v[164:167], v[200:203], v[122:125]
	v_mfma_i32_16x16x64_i8 v[110:113], v[156:159], v[208:211], v[110:113]
	v_mfma_i32_16x16x64_i8 v[106:109], v[164:167], v[208:211], v[106:109]
	v_mfma_i32_16x16x64_i8 v[94:97], v[156:159], v[216:219], v[94:97]
	v_mfma_i32_16x16x64_i8 v[90:93], v[164:167], v[216:219], v[90:93]
	v_mfma_i32_16x16x64_i8 v[78:81], v[156:159], v[224:227], v[78:81]
	v_mfma_i32_16x16x64_i8 v[74:77], v[164:167], v[224:227], v[74:77]
	s_setprio 0
	s_setprio 1
	v_mfma_i32_16x16x64_i8 v[118:121], v[168:171], v[196:199], v[118:121]
	v_mfma_i32_16x16x64_i8 v[114:117], v[186:189], v[196:199], v[114:117]
	v_mfma_i32_16x16x64_i8 v[102:105], v[168:171], v[204:207], v[102:105]
	v_mfma_i32_16x16x64_i8 v[98:101], v[186:189], v[204:207], v[98:101]
	v_mfma_i32_16x16x64_i8 v[86:89], v[168:171], v[212:215], v[86:89]
	v_mfma_i32_16x16x64_i8 v[82:85], v[186:189], v[212:215], v[82:85]
	v_mfma_i32_16x16x64_i8 v[70:73], v[168:171], v[220:223], v[70:73]
	v_mfma_i32_16x16x64_i8 v[66:69], v[186:189], v[220:223], v[66:69]
	v_mfma_i32_16x16x64_i8 v[118:121], v[182:185], v[200:203], v[118:121]
	v_mfma_i32_16x16x64_i8 v[114:117], v[190:193], v[200:203], v[114:117]
	v_mfma_i32_16x16x64_i8 v[102:105], v[182:185], v[208:211], v[102:105]
	v_mfma_i32_16x16x64_i8 v[98:101], v[190:193], v[208:211], v[98:101]
	v_mfma_i32_16x16x64_i8 v[86:89], v[182:185], v[216:219], v[86:89]
	v_mfma_i32_16x16x64_i8 v[82:85], v[190:193], v[216:219], v[82:85]
	v_mfma_i32_16x16x64_i8 v[70:73], v[182:185], v[224:227], v[70:73]
	v_mfma_i32_16x16x64_i8 v[66:69], v[190:193], v[224:227], v[66:69]
	s_setprio 0
	s_add_i32 s36, s62, s5
	v_lshl_add_u64 v[228:229], s[40:41], 0, v[134:135]
	s_mov_b32 m0, s36
	s_barrier
	ds_read_b128 v[196:199], v177 offset:16384
	ds_read_b128 v[200:203], v177 offset:17408
	ds_read_b128 v[204:207], v177 offset:18432
	ds_read_b128 v[208:211], v177 offset:19456
	ds_read_b128 v[212:215], v177 offset:20480
	ds_read_b128 v[216:219], v177 offset:21504
	ds_read_b128 v[220:223], v177 offset:22528
	ds_read_b128 v[224:227], v177 offset:23552
	global_load_lds_dwordx4 v[228:229], off
	s_add_i32 m0, s36, 0x2000
	s_add_u32 s36, s40, 0x40000
	v_lshl_add_u64 v[230:231], s[40:41], 0, v[132:133]
	s_addc_u32 s37, s41, 0
	s_add_i32 s68, s63, s5
	global_load_lds_dwordx4 v[230:231], off
	v_lshl_add_u64 v[232:233], s[36:37], 0, v[134:135]
	s_mov_b32 m0, s68
	s_nop 0
	global_load_lds_dwordx4 v[232:233], off
	v_lshl_add_u64 v[232:233], s[36:37], 0, v[132:133]
	s_add_i32 m0, s68, 0x2000
	s_and_b64 s[36:37], s[8:9], s[42:43]
	s_and_b64 s[36:37], s[36:37], exec
	s_cselect_b32 s36, s26, s34
	s_cselect_b32 s37, s27, s35
	s_add_u32 s36, s36, s70
	s_addc_u32 s37, s37, 0
	global_load_lds_dwordx4 v[232:233], off
	v_lshl_add_u64 v[232:233], s[36:37], 0, v[136:137]
	s_mov_b32 m0, s45
	v_lshl_add_u64 v[234:235], s[36:37], 0, v[138:139]
	global_load_lds_dwordx4 v[232:233], off
	s_mov_b32 m0, s46
	s_nop 0
	global_load_lds_dwordx4 v[234:235], off
	s_waitcnt vmcnt(8)
	s_waitcnt lgkmcnt(0)
	s_barrier
; #define PG8_LDA(dst, b, h) do { _Pragma("unroll") for (int m = 0; m < 4; ++m) dst[m] = PG8_LD32(lds + PG8_SA(b, h) + aoff + m * 2048); } while (0)
; #define PG8_LDB(dst, b, h) do { _Pragma("unroll") for (int n = 0; n < 2; ++n) dst[n] = PG8_LD32(lds + PG8_SB(b, h) + boff + n * 2048); } while (0)
; #define PG8_WAIT_V(n) asm volatile("s_waitcnt vmcnt(" #n ")" ::: "memory")
; #define PG8_WAIT_L(n) asm volatile("s_waitcnt lgkmcnt(" #n ")" ::: "memory")
; #define PG8_BAR __builtin_amdgcn_s_barrier()
; #define PG8_SCHED __builtin_amdgcn_sched_barrier(0)
; #define PG8_STA(bufoff, nextflag, h, koff) do { if constexpr (Sched::GATHER) { unsigned _o[2]; _o[0] = (nextflag) ? nxtA[h][0] : curA[h][0]; _o[1] = (nextflag) ? nxtA[h][1] : curA[h][1]; PG8_STAGE(bufoff, Ab + (koff), _o); } \
;         else { PG8_STAGE(bufoff, ((nextflag) ? nA : cA) + (size_t)(h) * hstep + (koff), voffA); } } while (0)
; template <class Epi, class Sched, bool ALIGN_EPI, int DT>
; __device__ __forceinline__ void gemm_phase(LAS unsigned char* lds, const int KB, const Sched& S, const Epi& E) {
;     ...
;             PG8_WAIT_V(8); PG8_WAIT_L(0); PG8_BAR; PG8_MMA(1, 0, At, B0); PG8_MMA(1, 1, At, B1); PG8_BAR; PG8_SCHED;
;             PG8_LDB(B0, 1, 0); PG8_LDB(B1, 1, 1); PG8_SCHED; PG8_LDA(At, 1, 0); PG8_STA(PG8_SA(0, 1), last, 1, k2);
;             PG8_WAIT_V(8); PG8_WAIT_L(0); PG8_BAR; PG8_MMA(0, 0, At, B0); PG8_MMA(0, 1, At, B1); PG8_BAR; PG8_SCHED;
	s_setprio 1
	s_waitcnt lgkmcnt(0)
	v_mfma_i32_16x16x64_i8 v[62:65], v[152:155], v[196:199], v[62:65]
	v_mfma_i32_16x16x64_i8 v[58:61], v[160:163], v[196:199], v[58:61]
	v_mfma_i32_16x16x64_i8 v[46:49], v[152:155], v[204:207], v[46:49]
	v_mfma_i32_16x16x64_i8 v[42:45], v[160:163], v[204:207], v[42:45]
	v_mfma_i32_16x16x64_i8 v[30:33], v[152:155], v[212:215], v[30:33]
	v_mfma_i32_16x16x64_i8 v[26:29], v[160:163], v[212:215], v[26:29]
	v_mfma_i32_16x16x64_i8 v[6:9], v[152:155], v[220:223], v[6:9]
	v_mfma_i32_16x16x64_i8 v[2:5], v[160:163], v[220:223], v[2:5]
	v_mfma_i32_16x16x64_i8 v[62:65], v[156:159], v[200:203], v[62:65]
	v_mfma_i32_16x16x64_i8 v[58:61], v[164:167], v[200:203], v[58:61]
	v_mfma_i32_16x16x64_i8 v[46:49], v[156:159], v[208:211], v[46:49]
	v_mfma_i32_16x16x64_i8 v[42:45], v[164:167], v[208:211], v[42:45]
	v_mfma_i32_16x16x64_i8 v[30:33], v[156:159], v[216:219], v[30:33]
	v_mfma_i32_16x16x64_i8 v[26:29], v[164:167], v[216:219], v[26:29]
	v_mfma_i32_16x16x64_i8 v[6:9], v[156:159], v[224:227], v[6:9]
	v_mfma_i32_16x16x64_i8 v[2:5], v[164:167], v[224:227], v[2:5]
	s_setprio 0
	s_setprio 1
	v_mfma_i32_16x16x64_i8 v[54:57], v[168:171], v[196:199], v[54:57]
	v_mfma_i32_16x16x64_i8 v[50:53], v[186:189], v[196:199], v[50:53]
	v_mfma_i32_16x16x64_i8 v[38:41], v[168:171], v[204:207], v[38:41]
	v_mfma_i32_16x16x64_i8 v[34:37], v[186:189], v[204:207], v[34:37]
	v_mfma_i32_16x16x64_i8 v[14:17], v[168:171], v[212:215], v[14:17]
	v_mfma_i32_16x16x64_i8 v[10:13], v[186:189], v[212:215], v[10:13]
	v_mfma_i32_16x16x64_i8 v[22:25], v[168:171], v[220:223], v[22:25]
	v_mfma_i32_16x16x64_i8 v[18:21], v[186:189], v[220:223], v[18:21]
	v_mfma_i32_16x16x64_i8 v[54:57], v[182:185], v[200:203], v[54:57]
	v_mfma_i32_16x16x64_i8 v[50:53], v[190:193], v[200:203], v[50:53]
	v_mfma_i32_16x16x64_i8 v[38:41], v[182:185], v[208:211], v[38:41]
	v_mfma_i32_16x16x64_i8 v[34:37], v[190:193], v[208:211], v[34:37]
	v_mfma_i32_16x16x64_i8 v[14:17], v[182:185], v[216:219], v[14:17]
	v_mfma_i32_16x16x64_i8 v[10:13], v[190:193], v[216:219], v[10:13]
	v_mfma_i32_16x16x64_i8 v[22:25], v[182:185], v[224:227], v[22:25]
	v_mfma_i32_16x16x64_i8 v[18:21], v[190:193], v[224:227], v[18:21]
	s_setprio 0
	s_add_i32 s42, 0, 0x18000
	v_add_u32_e32 v1, s42, v173
	s_add_i32 s43, 0, 0x1c000
	s_barrier
	ds_read_b128 v[152:155], v1
	ds_read_b128 v[156:159], v1 offset:1024
	ds_read_b128 v[160:163], v1 offset:2048
	ds_read_b128 v[164:167], v1 offset:3072
	v_add_u32_e32 v1, s43, v173
	ds_read_b128 v[168:171], v1
	ds_read_b128 v[182:185], v1 offset:1024
	ds_read_b128 v[186:189], v1 offset:2048
	ds_read_b128 v[190:193], v1 offset:3072
	s_add_u32 s36, s36, 0x40000
	s_addc_u32 s37, s37, 0
	s_mov_b32 m0, s47
	v_lshl_add_u64 v[236:237], s[36:37], 0, v[136:137]
	ds_read_b128 v[196:199], v177 offset:32768
	ds_read_b128 v[200:203], v177 offset:33792
	ds_read_b128 v[204:207], v177 offset:34816
	ds_read_b128 v[208:211], v177 offset:35840
	ds_read_b128 v[212:215], v177 offset:36864
	ds_read_b128 v[216:219], v177 offset:37888
	ds_read_b128 v[220:223], v177 offset:38912
	ds_read_b128 v[224:227], v177 offset:39936
	global_load_lds_dwordx4 v[236:237], off
	v_lshl_add_u64 v[236:237], s[36:37], 0, v[138:139]
	s_mov_b32 m0, s49
	s_nop 0
	global_load_lds_dwordx4 v[236:237], off
	s_waitcnt vmcnt(8)
	s_waitcnt lgkmcnt(0)
	s_barrier
	s_setprio 1
	s_waitcnt lgkmcnt(0)
	v_mfma_i32_16x16x64_i8 v[126:129], v[152:155], v[196:199], v[126:129]
	v_mfma_i32_16x16x64_i8 v[122:125], v[160:163], v[196:199], v[122:125]
	v_mfma_i32_16x16x64_i8 v[110:113], v[152:155], v[204:207], v[110:113]
	v_mfma_i32_16x16x64_i8 v[106:109], v[160:163], v[204:207], v[106:109]
	v_mfma_i32_16x16x64_i8 v[94:97], v[152:155], v[212:215], v[94:97]
	v_mfma_i32_16x16x64_i8 v[90:93], v[160:163], v[212:215], v[90:93]
	v_mfma_i32_16x16x64_i8 v[78:81], v[152:155], v[220:223], v[78:81]
	v_mfma_i32_16x16x64_i8 v[74:77], v[160:163], v[220:223], v[74:77]
	v_mfma_i32_16x16x64_i8 v[126:129], v[156:159], v[200:203], v[126:129]
	v_mfma_i32_16x16x64_i8 v[122:125], v[164:167], v[200:203], v[122:125]
	v_mfma_i32_16x16x64_i8 v[110:113], v[156:159], v[208:211], v[110:113]
	v_mfma_i32_16x16x64_i8 v[106:109], v[164:167], v[208:211], v[106:109]
	v_mfma_i32_16x16x64_i8 v[94:97], v[156:159], v[216:219], v[94:97]
	v_mfma_i32_16x16x64_i8 v[90:93], v[164:167], v[216:219], v[90:93]
	v_mfma_i32_16x16x64_i8 v[78:81], v[156:159], v[224:227], v[78:81]
	v_mfma_i32_16x16x64_i8 v[74:77], v[164:167], v[224:227], v[74:77]
	s_setprio 0
	s_setprio 1
	v_mfma_i32_16x16x64_i8 v[118:121], v[168:171], v[196:199], v[118:121]
	v_mfma_i32_16x16x64_i8 v[114:117], v[186:189], v[196:199], v[114:117]
	v_mfma_i32_16x16x64_i8 v[102:105], v[168:171], v[204:207], v[102:105]
	v_mfma_i32_16x16x64_i8 v[98:101], v[186:189], v[204:207], v[98:101]
	v_mfma_i32_16x16x64_i8 v[86:89], v[168:171], v[212:215], v[86:89]
	v_mfma_i32_16x16x64_i8 v[82:85], v[186:189], v[212:215], v[82:85]
	v_mfma_i32_16x16x64_i8 v[70:73], v[168:171], v[220:223], v[70:73]
	v_mfma_i32_16x16x64_i8 v[66:69], v[186:189], v[220:223], v[66:69]
	v_mfma_i32_16x16x64_i8 v[118:121], v[182:185], v[200:203], v[118:121]
	v_mfma_i32_16x16x64_i8 v[114:117], v[190:193], v[200:203], v[114:117]
	v_mfma_i32_16x16x64_i8 v[102:105], v[182:185], v[208:211], v[102:105]
	v_mfma_i32_16x16x64_i8 v[98:101], v[190:193], v[208:211], v[98:101]
	v_mfma_i32_16x16x64_i8 v[86:89], v[182:185], v[216:219], v[86:89]
	v_mfma_i32_16x16x64_i8 v[82:85], v[190:193], v[216:219], v[82:85]
	v_mfma_i32_16x16x64_i8 v[70:73], v[182:185], v[224:227], v[70:73]
	v_mfma_i32_16x16x64_i8 v[66:69], v[190:193], v[224:227], v[66:69]
	s_setprio 0
	s_add_i32 s36, s42, s5
	v_lshl_add_u64 v[228:229], v[228:229], 0, s[18:19]
	s_mov_b32 m0, s36
	s_barrier
; #define PG8_STAGE(bufoff, gbase, voff) do { _Pragma("unroll") for (int _i = 0; _i < 2; ++_i) \
;         __builtin_amdgcn_global_load_lds((const unsigned*)((const char*)(gbase) + (voff)[_i]), (LAS unsigned*)(lds + (bufoff) + ldsw + _i * 8192), 16, 0, 0); } while (0)
; #define PG8_LDA(dst, b, h) do { _Pragma("unroll") for (int m = 0; m < 4; ++m) dst[m] = PG8_LD32(lds + PG8_SA(b, h) + aoff + m * 2048); } while (0)
; #define PG8_WAIT_V(n) asm volatile("s_waitcnt vmcnt(" #n ")" ::: "memory")
; #define PG8_WAIT_L(n) asm volatile("s_waitcnt lgkmcnt(" #n ")" ::: "memory")
; #define PG8_BAR __builtin_amdgcn_s_barrier()
; #define PG8_SCHED __builtin_amdgcn_sched_barrier(0)
; #define PG8_STA(bufoff, nextflag, h, koff) do { if constexpr (Sched::GATHER) { unsigned _o[2]; _o[0] = (nextflag) ? nxtA[h][0] : curA[h][0]; _o[1] = (nextflag) ? nxtA[h][1] : curA[h][1]; PG8_STAGE(bufoff, Ab + (koff), _o); } \
;         else { PG8_STAGE(bufoff, ((nextflag) ? nA : cA) + (size_t)(h) * hstep + (koff), voffA); } } while (0)
; template <class Epi, class Sched, bool ALIGN_EPI, int DT>
; __device__ __forceinline__ void gemm_phase(LAS unsigned char* lds, const int KB, const Sched& S, const Epi& E) {
;     ...
;         for (int t = 0; t < nt; t += 2) {
;             const bool last = (t == nt - 2);
;             const size_t k1 = (size_t)(t + 1) * kstep, k2 = last ? 0 : (size_t)(t + 2) * kstep, k3 = k2 + kstep;
;     ...
;             PG8_LDA(At, 1, 1); PG8_STAGE(PG8_SB(1, 0), b3, voffB); PG8_STAGE(PG8_SB(1, 1), b3 + hstep, voffB); PG8_STA(PG8_SA(1, 0), last, 0, k3);
;             PG8_WAIT_V(8); PG8_WAIT_L(0); PG8_BAR; PG8_MMA(1, 0, At, B0); PG8_MMA(1, 1, At, B1); PG8_BAR; PG8_SCHED;
	ds_read_b128 v[196:199], v177 offset:49152
	ds_read_b128 v[200:203], v177 offset:50176
	ds_read_b128 v[204:207], v177 offset:51200
	ds_read_b128 v[208:211], v177 offset:52224
	ds_read_b128 v[212:215], v177 offset:53248
	ds_read_b128 v[216:219], v177 offset:54272
	ds_read_b128 v[220:223], v177 offset:55296
	ds_read_b128 v[224:227], v177 offset:56320
	global_load_lds_dwordx4 v[228:229], off
	s_add_i32 m0, s36, 0x2000
	s_add_u32 s36, s40, 0x40080
	v_lshl_add_u64 v[228:229], v[230:231], 0, s[18:19]
	s_addc_u32 s37, s41, 0
	s_add_i32 s40, s43, s5
	global_load_lds_dwordx4 v[228:229], off
	v_lshl_add_u64 v[228:229], s[36:37], 0, v[134:135]
	s_mov_b32 m0, s40
	s_nop 0
	global_load_lds_dwordx4 v[228:229], off
	v_lshl_add_u64 v[228:229], s[36:37], 0, v[132:133]
	s_add_i32 m0, s40, 0x2000
	s_nop 0
	global_load_lds_dwordx4 v[228:229], off
	v_lshl_add_u64 v[228:229], v[232:233], 0, s[18:19]
	s_mov_b32 m0, s55
	s_nop 0
	global_load_lds_dwordx4 v[228:229], off
	v_lshl_add_u64 v[228:229], v[234:235], 0, s[18:19]
	s_mov_b32 m0, s56
	s_nop 0
	global_load_lds_dwordx4 v[228:229], off
	s_waitcnt vmcnt(8)
	s_waitcnt lgkmcnt(0)
	s_barrier
	s_setprio 1
	s_waitcnt lgkmcnt(0)
	v_mfma_i32_16x16x64_i8 v[62:65], v[152:155], v[196:199], v[62:65]
	v_mfma_i32_16x16x64_i8 v[58:61], v[160:163], v[196:199], v[58:61]
	v_mfma_i32_16x16x64_i8 v[46:49], v[152:155], v[204:207], v[46:49]
	v_mfma_i32_16x16x64_i8 v[42:45], v[160:163], v[204:207], v[42:45]
	v_mfma_i32_16x16x64_i8 v[30:33], v[152:155], v[212:215], v[30:33]
	v_mfma_i32_16x16x64_i8 v[26:29], v[160:163], v[212:215], v[26:29]
	v_mfma_i32_16x16x64_i8 v[6:9], v[152:155], v[220:223], v[6:9]
	v_mfma_i32_16x16x64_i8 v[2:5], v[160:163], v[220:223], v[2:5]
	v_mfma_i32_16x16x64_i8 v[62:65], v[156:159], v[200:203], v[62:65]
	v_mfma_i32_16x16x64_i8 v[58:61], v[164:167], v[200:203], v[58:61]
	v_mfma_i32_16x16x64_i8 v[46:49], v[156:159], v[208:211], v[46:49]
	v_mfma_i32_16x16x64_i8 v[42:45], v[164:167], v[208:211], v[42:45]
	v_mfma_i32_16x16x64_i8 v[30:33], v[156:159], v[216:219], v[30:33]
	v_mfma_i32_16x16x64_i8 v[26:29], v[164:167], v[216:219], v[26:29]
	v_mfma_i32_16x16x64_i8 v[6:9], v[156:159], v[224:227], v[6:9]
	v_mfma_i32_16x16x64_i8 v[2:5], v[164:167], v[224:227], v[2:5]
	s_setprio 0
	s_setprio 1
	v_mfma_i32_16x16x64_i8 v[54:57], v[168:171], v[196:199], v[54:57]
	v_mfma_i32_16x16x64_i8 v[50:53], v[186:189], v[196:199], v[50:53]
	v_mfma_i32_16x16x64_i8 v[38:41], v[168:171], v[204:207], v[38:41]
	v_mfma_i32_16x16x64_i8 v[34:37], v[186:189], v[204:207], v[34:37]
	v_mfma_i32_16x16x64_i8 v[14:17], v[168:171], v[212:215], v[14:17]
	v_mfma_i32_16x16x64_i8 v[10:13], v[186:189], v[212:215], v[10:13]
	v_mfma_i32_16x16x64_i8 v[22:25], v[168:171], v[220:223], v[22:25]
	v_mfma_i32_16x16x64_i8 v[18:21], v[186:189], v[220:223], v[18:21]
	v_mfma_i32_16x16x64_i8 v[54:57], v[182:185], v[200:203], v[54:57]
	v_mfma_i32_16x16x64_i8 v[50:53], v[190:193], v[200:203], v[50:53]
	v_mfma_i32_16x16x64_i8 v[38:41], v[182:185], v[208:211], v[38:41]
	v_mfma_i32_16x16x64_i8 v[34:37], v[190:193], v[208:211], v[34:37]
	v_mfma_i32_16x16x64_i8 v[14:17], v[182:185], v[216:219], v[14:17]
	v_mfma_i32_16x16x64_i8 v[10:13], v[190:193], v[216:219], v[10:13]
	v_mfma_i32_16x16x64_i8 v[22:25], v[182:185], v[224:227], v[22:25]
	v_mfma_i32_16x16x64_i8 v[18:21], v[190:193], v[224:227], v[18:21]
	s_setprio 0
	s_add_i32 s67, s67, 2
	s_cmp_gt_u32 s67, 13
	s_mov_b64 s[36:37], s[38:39]
	s_barrier
	s_cbranch_scc0 .LBB0_193
	s_and_b64 vcc, exec, s[20:21]
	s_cbranch_vccz .LBB0_196
	s_barrier

.LBB0_1018:
	ds_read_b128 v[18:21], v193
	ds_read_b128 v[22:25], v193 offset:1024
	ds_read_b128 v[26:29], v193 offset:2048
	ds_read_b128 v[30:33], v193 offset:3072
	ds_read_b128 v[2:5], v195
	ds_read_b128 v[6:9], v195 offset:1024
	ds_read_b128 v[10:13], v195 offset:2048
	ds_read_b128 v[14:17], v195 offset:3072
	s_add_u32 s34, s38, 0x100
	s_addc_u32 s35, s39, 0
	s_add_u32 s68, s63, s38
	s_addc_u32 s69, s66, s39
	s_cmp_eq_u32 s67, 12
	s_cselect_b64 s[40:41], -1, 0
	s_and_b64 s[36:37], s[40:41], exec
	s_cselect_b32 s37, s21, s69
	s_cselect_b32 s36, s23, s68
	s_cselect_b32 s68, 0, s35
	s_cselect_b32 s69, 0, s34
	v_lshl_add_u64 v[222:223], v[178:179], 0, s[38:39]
	s_add_i32 m0, s29, 0xc000
	ds_read_b128 v[182:185], v196
	ds_read_b128 v[186:189], v196 offset:1024
	ds_read_b128 v[198:201], v196 offset:2048
	ds_read_b128 v[202:205], v196 offset:3072
	ds_read_b128 v[206:209], v196 offset:4096
	ds_read_b128 v[210:213], v196 offset:5120
	ds_read_b128 v[214:217], v196 offset:6144
	ds_read_b128 v[218:221], v196 offset:7168
	global_load_lds_dwordx4 v[222:223], off
	v_lshl_add_u64 v[222:223], v[180:181], 0, s[38:39]
	s_add_i32 m0, s29, 0xe000
	s_nop 0
	global_load_lds_dwordx4 v[222:223], off
	s_waitcnt vmcnt(8)
	s_waitcnt lgkmcnt(0)
	s_barrier
	s_setprio 1
	s_waitcnt lgkmcnt(0)
	v_mfma_scale_f32_16x16x128_f8f6f4 v[158:161], v[18:25], v[182:189], v[158:161], v190, v190 op_sel_hi:[0,0,0]
	v_mfma_scale_f32_16x16x128_f8f6f4 v[154:157], v[26:33], v[182:189], v[154:157], v190, v190 op_sel_hi:[0,0,0]
	v_mfma_scale_f32_16x16x128_f8f6f4 v[150:153], v[18:25], v[198:205], v[150:153], v190, v190 op_sel_hi:[0,0,0]
	v_mfma_scale_f32_16x16x128_f8f6f4 v[142:145], v[26:33], v[198:205], v[142:145], v190, v190 op_sel_hi:[0,0,0]
	v_mfma_scale_f32_16x16x128_f8f6f4 v[134:137], v[18:25], v[206:213], v[134:137], v190, v190 op_sel_hi:[0,0,0]
	v_mfma_scale_f32_16x16x128_f8f6f4 v[126:129], v[26:33], v[206:213], v[126:129], v190, v190 op_sel_hi:[0,0,0]
	v_mfma_scale_f32_16x16x128_f8f6f4 v[118:121], v[18:25], v[214:221], v[118:121], v190, v190 op_sel_hi:[0,0,0]
	v_mfma_scale_f32_16x16x128_f8f6f4 v[110:113], v[26:33], v[214:221], v[110:113], v190, v190 op_sel_hi:[0,0,0]
	s_setprio 0
	s_setprio 1
	v_mfma_scale_f32_16x16x128_f8f6f4 v[146:149], v[2:9], v[182:189], v[146:149], v190, v190 op_sel_hi:[0,0,0]
	v_mfma_scale_f32_16x16x128_f8f6f4 v[138:141], v[10:17], v[182:189], v[138:141], v190, v190 op_sel_hi:[0,0,0]
	v_mfma_scale_f32_16x16x128_f8f6f4 v[130:133], v[2:9], v[198:205], v[130:133], v190, v190 op_sel_hi:[0,0,0]
	v_mfma_scale_f32_16x16x128_f8f6f4 v[122:125], v[10:17], v[198:205], v[122:125], v190, v190 op_sel_hi:[0,0,0]
	v_mfma_scale_f32_16x16x128_f8f6f4 v[114:117], v[2:9], v[206:213], v[114:117], v190, v190 op_sel_hi:[0,0,0]
	v_mfma_scale_f32_16x16x128_f8f6f4 v[106:109], v[10:17], v[206:213], v[106:109], v190, v190 op_sel_hi:[0,0,0]
	v_mfma_scale_f32_16x16x128_f8f6f4 v[102:105], v[2:9], v[214:221], v[102:105], v190, v190 op_sel_hi:[0,0,0]
	v_mfma_scale_f32_16x16x128_f8f6f4 v[98:101], v[10:17], v[214:221], v[98:101], v190, v190 op_sel_hi:[0,0,0]
	s_setprio 0
	s_add_i32 s38, s53, s42
	v_lshl_add_u64 v[182:183], s[36:37], 0, v[162:163]
	s_mov_b32 m0, s38
	s_barrier
	ds_read_b128 v[198:201], v196 offset:16384
	ds_read_b128 v[202:205], v196 offset:17408
	ds_read_b128 v[206:209], v196 offset:18432
	ds_read_b128 v[210:213], v196 offset:19456
	ds_read_b128 v[214:217], v196 offset:20480
	ds_read_b128 v[218:221], v196 offset:21504
	ds_read_b128 v[222:225], v196 offset:22528
	ds_read_b128 v[226:229], v196 offset:23552
	global_load_lds_dwordx4 v[182:183], off
	s_add_i32 m0, s38, 0x2000
	s_add_u32 s38, s36, 0x40000
	v_lshl_add_u64 v[184:185], s[36:37], 0, v[164:165]
	s_addc_u32 s39, s37, 0
	s_add_i32 s70, s54, s42
	global_load_lds_dwordx4 v[184:185], off
	v_lshl_add_u64 v[186:187], s[38:39], 0, v[162:163]
	s_mov_b32 m0, s70
	s_nop 0
	global_load_lds_dwordx4 v[186:187], off
	v_lshl_add_u64 v[186:187], s[38:39], 0, v[164:165]
	s_add_i32 m0, s70, 0x2000
	s_and_b64 s[38:39], s[6:7], s[40:41]
	s_and_b64 s[38:39], s[38:39], exec
	s_cselect_b32 s38, s24, s30
	s_cselect_b32 s39, s25, s31
	s_add_u32 s38, s38, s69
	s_addc_u32 s39, s39, s68
	global_load_lds_dwordx4 v[186:187], off
	v_lshl_add_u64 v[186:187], s[38:39], 0, v[166:167]
	s_mov_b32 m0, s29
	v_lshl_add_u64 v[188:189], s[38:39], 0, v[168:169]
	global_load_lds_dwordx4 v[186:187], off
	s_mov_b32 m0, s43
	s_nop 0
	global_load_lds_dwordx4 v[188:189], off
	s_waitcnt vmcnt(8)
	s_waitcnt lgkmcnt(0)
	s_barrier
	s_setprio 1
	s_waitcnt lgkmcnt(0)
	v_mfma_scale_f32_16x16x128_f8f6f4 v[94:97], v[18:25], v[198:205], v[94:97], v190, v190 op_sel_hi:[0,0,0]
	v_mfma_scale_f32_16x16x128_f8f6f4 v[90:93], v[26:33], v[198:205], v[90:93], v190, v190 op_sel_hi:[0,0,0]
	v_mfma_scale_f32_16x16x128_f8f6f4 v[86:89], v[18:25], v[206:213], v[86:89], v190, v190 op_sel_hi:[0,0,0]
	v_mfma_scale_f32_16x16x128_f8f6f4 v[78:81], v[26:33], v[206:213], v[78:81], v190, v190 op_sel_hi:[0,0,0]
	v_mfma_scale_f32_16x16x128_f8f6f4 v[62:65], v[18:25], v[214:221], v[62:65], v190, v190 op_sel_hi:[0,0,0]
	v_mfma_scale_f32_16x16x128_f8f6f4 v[54:57], v[26:33], v[214:221], v[54:57], v190, v190 op_sel_hi:[0,0,0]
	v_mfma_scale_f32_16x16x128_f8f6f4 v[46:49], v[18:25], v[222:229], v[46:49], v190, v190 op_sel_hi:[0,0,0]
	v_mfma_scale_f32_16x16x128_f8f6f4 v[38:41], v[26:33], v[222:229], v[38:41], v190, v190 op_sel_hi:[0,0,0]
	s_setprio 0
	s_setprio 1
	v_mfma_scale_f32_16x16x128_f8f6f4 v[82:85], v[2:9], v[198:205], v[82:85], v190, v190 op_sel_hi:[0,0,0]
	v_mfma_scale_f32_16x16x128_f8f6f4 v[74:77], v[10:17], v[198:205], v[74:77], v190, v190 op_sel_hi:[0,0,0]
	v_mfma_scale_f32_16x16x128_f8f6f4 v[58:61], v[2:9], v[206:213], v[58:61], v190, v190 op_sel_hi:[0,0,0]
	v_mfma_scale_f32_16x16x128_f8f6f4 v[50:53], v[10:17], v[206:213], v[50:53], v190, v190 op_sel_hi:[0,0,0]
	v_mfma_scale_f32_16x16x128_f8f6f4 v[42:45], v[2:9], v[214:221], v[42:45], v190, v190 op_sel_hi:[0,0,0]
	v_mfma_scale_f32_16x16x128_f8f6f4 v[34:37], v[10:17], v[214:221], v[34:37], v190, v190 op_sel_hi:[0,0,0]
	v_mfma_scale_f32_16x16x128_f8f6f4 v[70:73], v[2:9], v[222:229], v[70:73], v190, v190 op_sel_hi:[0,0,0]
	v_mfma_scale_f32_16x16x128_f8f6f4 v[66:69], v[10:17], v[222:229], v[66:69], v190, v190 op_sel_hi:[0,0,0]
	s_setprio 0
	s_add_i32 s40, 0, 0x18000
	s_add_i32 s41, 0, 0x1c000
	v_add_u32_e32 v14, s40, v191
	v_add_u32_e32 v30, s41, v191
	s_barrier
	ds_read_b128 v[2:5], v14
	ds_read_b128 v[6:9], v14 offset:1024
	ds_read_b128 v[10:13], v14 offset:2048
	ds_read_b128 v[14:17], v14 offset:3072
	ds_read_b128 v[18:21], v30
	ds_read_b128 v[22:25], v30 offset:1024
	ds_read_b128 v[26:29], v30 offset:2048
	ds_read_b128 v[30:33], v30 offset:3072
	s_add_u32 s38, s38, 0x40000
	s_addc_u32 s39, s39, 0
	s_mov_b32 m0, s44
	v_lshl_add_u64 v[230:231], s[38:39], 0, v[166:167]
	ds_read_b128 v[198:201], v196 offset:32768
	ds_read_b128 v[202:205], v196 offset:33792
	ds_read_b128 v[206:209], v196 offset:34816
	ds_read_b128 v[210:213], v196 offset:35840
	ds_read_b128 v[214:217], v196 offset:36864
	ds_read_b128 v[218:221], v196 offset:37888
	ds_read_b128 v[222:225], v196 offset:38912
	ds_read_b128 v[226:229], v196 offset:39936
	global_load_lds_dwordx4 v[230:231], off
	v_lshl_add_u64 v[230:231], s[38:39], 0, v[168:169]
	s_mov_b32 m0, s45
	s_nop 0
	global_load_lds_dwordx4 v[230:231], off
	s_waitcnt vmcnt(8)
	s_waitcnt lgkmcnt(0)
	s_barrier
	s_setprio 1
	s_waitcnt lgkmcnt(0)
	v_mfma_scale_f32_16x16x128_f8f6f4 v[158:161], v[2:9], v[198:205], v[158:161], v190, v190 op_sel_hi:[0,0,0]
	v_mfma_scale_f32_16x16x128_f8f6f4 v[154:157], v[10:17], v[198:205], v[154:157], v190, v190 op_sel_hi:[0,0,0]
	v_mfma_scale_f32_16x16x128_f8f6f4 v[150:153], v[2:9], v[206:213], v[150:153], v190, v190 op_sel_hi:[0,0,0]
	v_mfma_scale_f32_16x16x128_f8f6f4 v[142:145], v[10:17], v[206:213], v[142:145], v190, v190 op_sel_hi:[0,0,0]
	v_mfma_scale_f32_16x16x128_f8f6f4 v[134:137], v[2:9], v[214:221], v[134:137], v190, v190 op_sel_hi:[0,0,0]
	v_mfma_scale_f32_16x16x128_f8f6f4 v[126:129], v[10:17], v[214:221], v[126:129], v190, v190 op_sel_hi:[0,0,0]
	v_mfma_scale_f32_16x16x128_f8f6f4 v[118:121], v[2:9], v[222:229], v[118:121], v190, v190 op_sel_hi:[0,0,0]
	v_mfma_scale_f32_16x16x128_f8f6f4 v[110:113], v[10:17], v[222:229], v[110:113], v190, v190 op_sel_hi:[0,0,0]
	s_setprio 0
	s_setprio 1
	v_mfma_scale_f32_16x16x128_f8f6f4 v[146:149], v[18:25], v[198:205], v[146:149], v190, v190 op_sel_hi:[0,0,0]
	v_mfma_scale_f32_16x16x128_f8f6f4 v[138:141], v[26:33], v[198:205], v[138:141], v190, v190 op_sel_hi:[0,0,0]
	v_mfma_scale_f32_16x16x128_f8f6f4 v[130:133], v[18:25], v[206:213], v[130:133], v190, v190 op_sel_hi:[0,0,0]
	v_mfma_scale_f32_16x16x128_f8f6f4 v[122:125], v[26:33], v[206:213], v[122:125], v190, v190 op_sel_hi:[0,0,0]
	v_mfma_scale_f32_16x16x128_f8f6f4 v[114:117], v[18:25], v[214:221], v[114:117], v190, v190 op_sel_hi:[0,0,0]
	v_mfma_scale_f32_16x16x128_f8f6f4 v[106:109], v[26:33], v[214:221], v[106:109], v190, v190 op_sel_hi:[0,0,0]
	v_mfma_scale_f32_16x16x128_f8f6f4 v[102:105], v[18:25], v[222:229], v[102:105], v190, v190 op_sel_hi:[0,0,0]
	v_mfma_scale_f32_16x16x128_f8f6f4 v[98:101], v[26:33], v[222:229], v[98:101], v190, v190 op_sel_hi:[0,0,0]
	s_setprio 0
	s_add_i32 s38, s40, s42
	v_lshl_add_u64 v[182:183], v[182:183], 0, s[10:11]
	s_mov_b32 m0, s38
	s_barrier
	ds_read_b128 v[198:201], v196 offset:49152
	ds_read_b128 v[202:205], v196 offset:50176
	ds_read_b128 v[206:209], v196 offset:51200
	ds_read_b128 v[210:213], v196 offset:52224
	ds_read_b128 v[214:217], v196 offset:53248
	ds_read_b128 v[218:221], v196 offset:54272
	ds_read_b128 v[222:225], v196 offset:55296
	ds_read_b128 v[226:229], v196 offset:56320
	global_load_lds_dwordx4 v[182:183], off
	s_add_i32 m0, s38, 0x2000
	s_add_u32 s36, s36, 0x40080
	v_lshl_add_u64 v[182:183], v[184:185], 0, s[10:11]
	s_addc_u32 s37, s37, 0
	s_add_i32 s38, s41, s42
	global_load_lds_dwordx4 v[182:183], off
	v_lshl_add_u64 v[182:183], s[36:37], 0, v[162:163]
	s_mov_b32 m0, s38
	s_nop 0
	global_load_lds_dwordx4 v[182:183], off
	v_lshl_add_u64 v[182:183], s[36:37], 0, v[164:165]
	s_add_i32 m0, s38, 0x2000
	s_nop 0
	global_load_lds_dwordx4 v[182:183], off
	v_lshl_add_u64 v[182:183], v[186:187], 0, s[10:11]
	s_mov_b32 m0, s47
	s_nop 0
	global_load_lds_dwordx4 v[182:183], off
	v_lshl_add_u64 v[182:183], v[188:189], 0, s[10:11]
	s_mov_b32 m0, s49
	s_nop 0
	global_load_lds_dwordx4 v[182:183], off
	s_waitcnt vmcnt(8)
	s_waitcnt lgkmcnt(0)
	s_barrier
	s_setprio 1
	s_waitcnt lgkmcnt(0)
	v_mfma_scale_f32_16x16x128_f8f6f4 v[94:97], v[2:9], v[198:205], v[94:97], v190, v190 op_sel_hi:[0,0,0]
	v_mfma_scale_f32_16x16x128_f8f6f4 v[90:93], v[10:17], v[198:205], v[90:93], v190, v190 op_sel_hi:[0,0,0]
	v_mfma_scale_f32_16x16x128_f8f6f4 v[86:89], v[2:9], v[206:213], v[86:89], v190, v190 op_sel_hi:[0,0,0]
	v_mfma_scale_f32_16x16x128_f8f6f4 v[78:81], v[10:17], v[206:213], v[78:81], v190, v190 op_sel_hi:[0,0,0]
	v_mfma_scale_f32_16x16x128_f8f6f4 v[62:65], v[2:9], v[214:221], v[62:65], v190, v190 op_sel_hi:[0,0,0]
	v_mfma_scale_f32_16x16x128_f8f6f4 v[54:57], v[10:17], v[214:221], v[54:57], v190, v190 op_sel_hi:[0,0,0]
	v_mfma_scale_f32_16x16x128_f8f6f4 v[46:49], v[2:9], v[222:229], v[46:49], v190, v190 op_sel_hi:[0,0,0]
	v_mfma_scale_f32_16x16x128_f8f6f4 v[38:41], v[10:17], v[222:229], v[38:41], v190, v190 op_sel_hi:[0,0,0]
	s_setprio 0
	s_setprio 1
	v_mfma_scale_f32_16x16x128_f8f6f4 v[82:85], v[18:25], v[198:205], v[82:85], v190, v190 op_sel_hi:[0,0,0]
	v_mfma_scale_f32_16x16x128_f8f6f4 v[74:77], v[26:33], v[198:205], v[74:77], v190, v190 op_sel_hi:[0,0,0]
	v_mfma_scale_f32_16x16x128_f8f6f4 v[58:61], v[18:25], v[206:213], v[58:61], v190, v190 op_sel_hi:[0,0,0]
	v_mfma_scale_f32_16x16x128_f8f6f4 v[50:53], v[26:33], v[206:213], v[50:53], v190, v190 op_sel_hi:[0,0,0]
	v_mfma_scale_f32_16x16x128_f8f6f4 v[42:45], v[18:25], v[214:221], v[42:45], v190, v190 op_sel_hi:[0,0,0]
	v_mfma_scale_f32_16x16x128_f8f6f4 v[34:37], v[26:33], v[214:221], v[34:37], v190, v190 op_sel_hi:[0,0,0]
	v_mfma_scale_f32_16x16x128_f8f6f4 v[70:73], v[18:25], v[222:229], v[70:73], v190, v190 op_sel_hi:[0,0,0]
	v_mfma_scale_f32_16x16x128_f8f6f4 v[66:69], v[26:33], v[222:229], v[66:69], v190, v190 op_sel_hi:[0,0,0]
	s_setprio 0
	s_add_i32 s67, s67, 2
	s_cmp_gt_u32 s67, 13
	s_mov_b64 s[38:39], s[34:35]
	s_barrier
	s_cbranch_scc0 .LBB0_1018
	s_and_b64 vcc, exec, s[12:13]
	s_cbranch_vccz .LBB0_1021
	s_barrier

.LBB0_1154:
	ds_read_b128 v[70:73], v167
	ds_read_b128 v[156:159], v167 offset:1024
	ds_read_b128 v[160:163], v167 offset:2048
	ds_read_b128 v[172:175], v167 offset:3072
	ds_read_b128 v[176:179], v168
	ds_read_b128 v[180:183], v168 offset:1024
	ds_read_b128 v[184:187], v168 offset:2048
	ds_read_b128 v[188:191], v168 offset:3072
	s_add_u32 s30, s28, 0x100
	s_addc_u32 s31, s29, 0
	s_add_u32 s63, s56, s28
	s_addc_u32 s66, s57, s29
	s_cmp_eq_u32 s62, 12
	s_cselect_b64 s[36:37], -1, 0
	s_and_b64 s[34:35], s[36:37], exec
	s_cselect_b32 s67, 0, s30
	s_cselect_b32 s35, s17, s66
	s_cselect_b32 s34, s19, s63
	v_lshl_add_u64 v[192:193], v[66:67], 0, s[28:29]
	s_add_i32 m0, s25, 0xc000
	ds_read_b128 v[196:199], v169
	ds_read_b128 v[200:203], v169 offset:1024
	ds_read_b128 v[204:207], v169 offset:2048
	ds_read_b128 v[208:211], v169 offset:3072
	ds_read_b128 v[212:215], v169 offset:4096
	ds_read_b128 v[216:219], v169 offset:5120
	ds_read_b128 v[220:223], v169 offset:6144
	ds_read_b128 v[224:227], v169 offset:7168
	global_load_lds_dwordx4 v[192:193], off
	v_lshl_add_u64 v[192:193], v[68:69], 0, s[28:29]
	s_add_i32 m0, s25, 0xe000
	s_nop 0
	global_load_lds_dwordx4 v[192:193], off
	s_waitcnt vmcnt(8)
	s_waitcnt lgkmcnt(0)
	s_barrier
	s_setprio 1
	s_waitcnt lgkmcnt(0)
	v_mfma_i32_16x16x64_i8 v[134:137], v[70:73], v[196:199], v[134:137]
	v_mfma_i32_16x16x64_i8 v[126:129], v[160:163], v[196:199], v[126:129]
	v_mfma_i32_16x16x64_i8 v[118:121], v[70:73], v[204:207], v[118:121]
	v_mfma_i32_16x16x64_i8 v[110:113], v[160:163], v[204:207], v[110:113]
	v_mfma_i32_16x16x64_i8 v[102:105], v[70:73], v[212:215], v[102:105]
	v_mfma_i32_16x16x64_i8 v[94:97], v[160:163], v[212:215], v[94:97]
	v_mfma_i32_16x16x64_i8 v[86:89], v[70:73], v[220:223], v[86:89]
	v_mfma_i32_16x16x64_i8 v[78:81], v[160:163], v[220:223], v[78:81]
	v_mfma_i32_16x16x64_i8 v[134:137], v[156:159], v[200:203], v[134:137]
	v_mfma_i32_16x16x64_i8 v[126:129], v[172:175], v[200:203], v[126:129]
	v_mfma_i32_16x16x64_i8 v[118:121], v[156:159], v[208:211], v[118:121]
	v_mfma_i32_16x16x64_i8 v[110:113], v[172:175], v[208:211], v[110:113]
	v_mfma_i32_16x16x64_i8 v[102:105], v[156:159], v[216:219], v[102:105]
	v_mfma_i32_16x16x64_i8 v[94:97], v[172:175], v[216:219], v[94:97]
	v_mfma_i32_16x16x64_i8 v[86:89], v[156:159], v[224:227], v[86:89]
	v_mfma_i32_16x16x64_i8 v[78:81], v[172:175], v[224:227], v[78:81]
	s_setprio 0
	s_setprio 1
	v_mfma_i32_16x16x64_i8 v[130:133], v[176:179], v[196:199], v[130:133]
	v_mfma_i32_16x16x64_i8 v[122:125], v[184:187], v[196:199], v[122:125]
	v_mfma_i32_16x16x64_i8 v[114:117], v[176:179], v[204:207], v[114:117]
	v_mfma_i32_16x16x64_i8 v[106:109], v[184:187], v[204:207], v[106:109]
	v_mfma_i32_16x16x64_i8 v[98:101], v[176:179], v[212:215], v[98:101]
	v_mfma_i32_16x16x64_i8 v[90:93], v[184:187], v[212:215], v[90:93]
	v_mfma_i32_16x16x64_i8 v[82:85], v[176:179], v[220:223], v[82:85]
	v_mfma_i32_16x16x64_i8 v[74:77], v[184:187], v[220:223], v[74:77]
	v_mfma_i32_16x16x64_i8 v[130:133], v[180:183], v[200:203], v[130:133]
	v_mfma_i32_16x16x64_i8 v[122:125], v[188:191], v[200:203], v[122:125]
	v_mfma_i32_16x16x64_i8 v[114:117], v[180:183], v[208:211], v[114:117]
	v_mfma_i32_16x16x64_i8 v[106:109], v[188:191], v[208:211], v[106:109]
	v_mfma_i32_16x16x64_i8 v[98:101], v[180:183], v[216:219], v[98:101]
	v_mfma_i32_16x16x64_i8 v[90:93], v[188:191], v[216:219], v[90:93]
	v_mfma_i32_16x16x64_i8 v[82:85], v[180:183], v[224:227], v[82:85]
	v_mfma_i32_16x16x64_i8 v[74:77], v[188:191], v[224:227], v[74:77]
	s_setprio 0
	s_add_i32 s28, s49, s38
	v_lshl_add_u64 v[192:193], s[34:35], 0, v[140:141]
	s_mov_b32 m0, s28
	s_barrier
	ds_read_b128 v[196:199], v169 offset:16384
	ds_read_b128 v[200:203], v169 offset:17408
	ds_read_b128 v[204:207], v169 offset:18432
	ds_read_b128 v[208:211], v169 offset:19456
	ds_read_b128 v[212:215], v169 offset:20480
	ds_read_b128 v[216:219], v169 offset:21504
	ds_read_b128 v[220:223], v169 offset:22528
	ds_read_b128 v[224:227], v169 offset:23552
	global_load_lds_dwordx4 v[192:193], off
	s_add_i32 m0, s28, 0x2000
	s_add_u32 s28, s34, 0x40000
	v_lshl_add_u64 v[228:229], s[34:35], 0, v[138:139]
	s_addc_u32 s29, s35, 0
	s_add_i32 s63, s52, s38
	global_load_lds_dwordx4 v[228:229], off
	v_lshl_add_u64 v[230:231], s[28:29], 0, v[140:141]
	s_mov_b32 m0, s63
	s_nop 0
	global_load_lds_dwordx4 v[230:231], off
	v_lshl_add_u64 v[230:231], s[28:29], 0, v[138:139]
	s_add_i32 m0, s63, 0x2000
	s_and_b64 s[28:29], s[6:7], s[36:37]
	s_and_b64 s[28:29], s[28:29], exec
	s_cselect_b32 s28, s20, s26
	s_cselect_b32 s29, s21, s27
	s_add_u32 s28, s28, s67
	s_addc_u32 s29, s29, 0
	global_load_lds_dwordx4 v[230:231], off
	v_lshl_add_u64 v[230:231], s[28:29], 0, v[142:143]
	s_mov_b32 m0, s25
	v_lshl_add_u64 v[232:233], s[28:29], 0, v[144:145]
	global_load_lds_dwordx4 v[230:231], off
	s_mov_b32 m0, s41
	s_nop 0
	global_load_lds_dwordx4 v[232:233], off
	s_waitcnt vmcnt(8)
	s_waitcnt lgkmcnt(0)
	s_barrier
	s_setprio 1
	s_waitcnt lgkmcnt(0)
	v_mfma_i32_16x16x64_i8 v[62:65], v[70:73], v[196:199], v[62:65]
	v_mfma_i32_16x16x64_i8 v[54:57], v[160:163], v[196:199], v[54:57]
	v_mfma_i32_16x16x64_i8 v[46:49], v[70:73], v[204:207], v[46:49]
	v_mfma_i32_16x16x64_i8 v[38:41], v[160:163], v[204:207], v[38:41]
	v_mfma_i32_16x16x64_i8 v[30:33], v[70:73], v[212:215], v[30:33]
	v_mfma_i32_16x16x64_i8 v[22:25], v[160:163], v[212:215], v[22:25]
	v_mfma_i32_16x16x64_i8 v[6:9], v[70:73], v[220:223], v[6:9]
	v_mfma_i32_16x16x64_i8 v[2:5], v[160:163], v[220:223], v[2:5]
	v_mfma_i32_16x16x64_i8 v[62:65], v[156:159], v[200:203], v[62:65]
	v_mfma_i32_16x16x64_i8 v[54:57], v[172:175], v[200:203], v[54:57]
	v_mfma_i32_16x16x64_i8 v[46:49], v[156:159], v[208:211], v[46:49]
	v_mfma_i32_16x16x64_i8 v[38:41], v[172:175], v[208:211], v[38:41]
	v_mfma_i32_16x16x64_i8 v[30:33], v[156:159], v[216:219], v[30:33]
	v_mfma_i32_16x16x64_i8 v[22:25], v[172:175], v[216:219], v[22:25]
	v_mfma_i32_16x16x64_i8 v[6:9], v[156:159], v[224:227], v[6:9]
	v_mfma_i32_16x16x64_i8 v[2:5], v[172:175], v[224:227], v[2:5]
	s_setprio 0
	s_setprio 1
	v_mfma_i32_16x16x64_i8 v[58:61], v[176:179], v[196:199], v[58:61]
	v_mfma_i32_16x16x64_i8 v[50:53], v[184:187], v[196:199], v[50:53]
	v_mfma_i32_16x16x64_i8 v[42:45], v[176:179], v[204:207], v[42:45]
	v_mfma_i32_16x16x64_i8 v[34:37], v[184:187], v[204:207], v[34:37]
	v_mfma_i32_16x16x64_i8 v[26:29], v[176:179], v[212:215], v[26:29]
	v_mfma_i32_16x16x64_i8 v[18:21], v[184:187], v[212:215], v[18:21]
	v_mfma_i32_16x16x64_i8 v[14:17], v[176:179], v[220:223], v[14:17]
	v_mfma_i32_16x16x64_i8 v[10:13], v[184:187], v[220:223], v[10:13]
	v_mfma_i32_16x16x64_i8 v[58:61], v[180:183], v[200:203], v[58:61]
	v_mfma_i32_16x16x64_i8 v[50:53], v[188:191], v[200:203], v[50:53]
	v_mfma_i32_16x16x64_i8 v[42:45], v[180:183], v[208:211], v[42:45]
	v_mfma_i32_16x16x64_i8 v[34:37], v[188:191], v[208:211], v[34:37]
	v_mfma_i32_16x16x64_i8 v[26:29], v[180:183], v[216:219], v[26:29]
	v_mfma_i32_16x16x64_i8 v[18:21], v[188:191], v[216:219], v[18:21]
	v_mfma_i32_16x16x64_i8 v[14:17], v[180:183], v[224:227], v[14:17]
	v_mfma_i32_16x16x64_i8 v[10:13], v[188:191], v[224:227], v[10:13]
	s_setprio 0
	s_add_i32 s36, 0, 0x18000
	v_add_u32_e32 v1, s36, v165
	s_add_i32 s37, 0, 0x1c000
	s_barrier
	ds_read_b128 v[70:73], v1
	ds_read_b128 v[156:159], v1 offset:1024
	ds_read_b128 v[160:163], v1 offset:2048
	ds_read_b128 v[172:175], v1 offset:3072
	v_add_u32_e32 v1, s37, v165
	ds_read_b128 v[176:179], v1
	ds_read_b128 v[180:183], v1 offset:1024
	ds_read_b128 v[184:187], v1 offset:2048
	ds_read_b128 v[188:191], v1 offset:3072
	s_add_u32 s28, s28, 0x40000
	s_addc_u32 s29, s29, 0
	s_mov_b32 m0, s42
	v_lshl_add_u64 v[234:235], s[28:29], 0, v[142:143]
	ds_read_b128 v[196:199], v169 offset:32768
	ds_read_b128 v[200:203], v169 offset:33792
	ds_read_b128 v[204:207], v169 offset:34816
	ds_read_b128 v[208:211], v169 offset:35840
	ds_read_b128 v[212:215], v169 offset:36864
	ds_read_b128 v[216:219], v169 offset:37888
	ds_read_b128 v[220:223], v169 offset:38912
	ds_read_b128 v[224:227], v169 offset:39936
	global_load_lds_dwordx4 v[234:235], off
	v_lshl_add_u64 v[234:235], s[28:29], 0, v[144:145]
	s_mov_b32 m0, s43
	s_nop 0
	global_load_lds_dwordx4 v[234:235], off
	s_waitcnt vmcnt(8)
	s_waitcnt lgkmcnt(0)
	s_barrier
	s_setprio 1
	s_waitcnt lgkmcnt(0)
	v_mfma_i32_16x16x64_i8 v[134:137], v[70:73], v[196:199], v[134:137]
	v_mfma_i32_16x16x64_i8 v[126:129], v[160:163], v[196:199], v[126:129]
	v_mfma_i32_16x16x64_i8 v[118:121], v[70:73], v[204:207], v[118:121]
	v_mfma_i32_16x16x64_i8 v[110:113], v[160:163], v[204:207], v[110:113]
	v_mfma_i32_16x16x64_i8 v[102:105], v[70:73], v[212:215], v[102:105]
	v_mfma_i32_16x16x64_i8 v[94:97], v[160:163], v[212:215], v[94:97]
	v_mfma_i32_16x16x64_i8 v[86:89], v[70:73], v[220:223], v[86:89]
	v_mfma_i32_16x16x64_i8 v[78:81], v[160:163], v[220:223], v[78:81]
	v_mfma_i32_16x16x64_i8 v[134:137], v[156:159], v[200:203], v[134:137]
	v_mfma_i32_16x16x64_i8 v[126:129], v[172:175], v[200:203], v[126:129]
	v_mfma_i32_16x16x64_i8 v[118:121], v[156:159], v[208:211], v[118:121]
	v_mfma_i32_16x16x64_i8 v[110:113], v[172:175], v[208:211], v[110:113]
	v_mfma_i32_16x16x64_i8 v[102:105], v[156:159], v[216:219], v[102:105]
	v_mfma_i32_16x16x64_i8 v[94:97], v[172:175], v[216:219], v[94:97]
	v_mfma_i32_16x16x64_i8 v[86:89], v[156:159], v[224:227], v[86:89]
	v_mfma_i32_16x16x64_i8 v[78:81], v[172:175], v[224:227], v[78:81]
	s_setprio 0
	s_setprio 1
	v_mfma_i32_16x16x64_i8 v[130:133], v[176:179], v[196:199], v[130:133]
	v_mfma_i32_16x16x64_i8 v[122:125], v[184:187], v[196:199], v[122:125]
	v_mfma_i32_16x16x64_i8 v[114:117], v[176:179], v[204:207], v[114:117]
	v_mfma_i32_16x16x64_i8 v[106:109], v[184:187], v[204:207], v[106:109]
	v_mfma_i32_16x16x64_i8 v[98:101], v[176:179], v[212:215], v[98:101]
	v_mfma_i32_16x16x64_i8 v[90:93], v[184:187], v[212:215], v[90:93]
	v_mfma_i32_16x16x64_i8 v[82:85], v[176:179], v[220:223], v[82:85]
	v_mfma_i32_16x16x64_i8 v[74:77], v[184:187], v[220:223], v[74:77]
	v_mfma_i32_16x16x64_i8 v[130:133], v[180:183], v[200:203], v[130:133]
	v_mfma_i32_16x16x64_i8 v[122:125], v[188:191], v[200:203], v[122:125]
	v_mfma_i32_16x16x64_i8 v[114:117], v[180:183], v[208:211], v[114:117]
	v_mfma_i32_16x16x64_i8 v[106:109], v[188:191], v[208:211], v[106:109]
	v_mfma_i32_16x16x64_i8 v[98:101], v[180:183], v[216:219], v[98:101]
	v_mfma_i32_16x16x64_i8 v[90:93], v[188:191], v[216:219], v[90:93]
	v_mfma_i32_16x16x64_i8 v[82:85], v[180:183], v[224:227], v[82:85]
	v_mfma_i32_16x16x64_i8 v[74:77], v[188:191], v[224:227], v[74:77]
	s_setprio 0
	s_add_i32 s28, s36, s38
	v_lshl_add_u64 v[192:193], v[192:193], 0, s[12:13]
	s_mov_b32 m0, s28
	s_barrier
	ds_read_b128 v[196:199], v169 offset:49152
	ds_read_b128 v[200:203], v169 offset:50176
	ds_read_b128 v[204:207], v169 offset:51200
	ds_read_b128 v[208:211], v169 offset:52224
	ds_read_b128 v[212:215], v169 offset:53248
	ds_read_b128 v[216:219], v169 offset:54272
	ds_read_b128 v[220:223], v169 offset:55296
	ds_read_b128 v[224:227], v169 offset:56320
	global_load_lds_dwordx4 v[192:193], off
	s_add_i32 m0, s28, 0x2000
	s_add_u32 s28, s34, 0x40080
	v_lshl_add_u64 v[192:193], v[228:229], 0, s[12:13]
	s_addc_u32 s29, s35, 0
	s_add_i32 s34, s37, s38
	global_load_lds_dwordx4 v[192:193], off
	v_lshl_add_u64 v[192:193], s[28:29], 0, v[140:141]
	s_mov_b32 m0, s34
	s_nop 0
	global_load_lds_dwordx4 v[192:193], off
	v_lshl_add_u64 v[192:193], s[28:29], 0, v[138:139]
	s_add_i32 m0, s34, 0x2000
	s_nop 0
	global_load_lds_dwordx4 v[192:193], off
	v_lshl_add_u64 v[192:193], v[230:231], 0, s[12:13]
	s_mov_b32 m0, s45
	s_nop 0
	global_load_lds_dwordx4 v[192:193], off
	v_lshl_add_u64 v[192:193], v[232:233], 0, s[12:13]
	s_mov_b32 m0, s46
	s_nop 0
	global_load_lds_dwordx4 v[192:193], off
	s_waitcnt vmcnt(8)
	s_waitcnt lgkmcnt(0)
	s_barrier
	s_setprio 1
	s_waitcnt lgkmcnt(0)
	v_mfma_i32_16x16x64_i8 v[62:65], v[70:73], v[196:199], v[62:65]
	v_mfma_i32_16x16x64_i8 v[54:57], v[160:163], v[196:199], v[54:57]
	v_mfma_i32_16x16x64_i8 v[46:49], v[70:73], v[204:207], v[46:49]
	v_mfma_i32_16x16x64_i8 v[38:41], v[160:163], v[204:207], v[38:41]
	v_mfma_i32_16x16x64_i8 v[30:33], v[70:73], v[212:215], v[30:33]
	v_mfma_i32_16x16x64_i8 v[22:25], v[160:163], v[212:215], v[22:25]
	v_mfma_i32_16x16x64_i8 v[6:9], v[70:73], v[220:223], v[6:9]
	v_mfma_i32_16x16x64_i8 v[2:5], v[160:163], v[220:223], v[2:5]
	v_mfma_i32_16x16x64_i8 v[62:65], v[156:159], v[200:203], v[62:65]
	v_mfma_i32_16x16x64_i8 v[54:57], v[172:175], v[200:203], v[54:57]
	v_mfma_i32_16x16x64_i8 v[46:49], v[156:159], v[208:211], v[46:49]
	v_mfma_i32_16x16x64_i8 v[38:41], v[172:175], v[208:211], v[38:41]
	v_mfma_i32_16x16x64_i8 v[30:33], v[156:159], v[216:219], v[30:33]
	v_mfma_i32_16x16x64_i8 v[22:25], v[172:175], v[216:219], v[22:25]
	v_mfma_i32_16x16x64_i8 v[6:9], v[156:159], v[224:227], v[6:9]
	v_mfma_i32_16x16x64_i8 v[2:5], v[172:175], v[224:227], v[2:5]
	s_setprio 0
	s_setprio 1
	v_mfma_i32_16x16x64_i8 v[58:61], v[176:179], v[196:199], v[58:61]
	v_mfma_i32_16x16x64_i8 v[50:53], v[184:187], v[196:199], v[50:53]
	v_mfma_i32_16x16x64_i8 v[42:45], v[176:179], v[204:207], v[42:45]
	v_mfma_i32_16x16x64_i8 v[34:37], v[184:187], v[204:207], v[34:37]
	v_mfma_i32_16x16x64_i8 v[26:29], v[176:179], v[212:215], v[26:29]
	v_mfma_i32_16x16x64_i8 v[18:21], v[184:187], v[212:215], v[18:21]
	v_mfma_i32_16x16x64_i8 v[14:17], v[176:179], v[220:223], v[14:17]
	v_mfma_i32_16x16x64_i8 v[10:13], v[184:187], v[220:223], v[10:13]
	v_mfma_i32_16x16x64_i8 v[58:61], v[180:183], v[200:203], v[58:61]
	v_mfma_i32_16x16x64_i8 v[50:53], v[188:191], v[200:203], v[50:53]
	v_mfma_i32_16x16x64_i8 v[42:45], v[180:183], v[208:211], v[42:45]
	v_mfma_i32_16x16x64_i8 v[34:37], v[188:191], v[208:211], v[34:37]
	v_mfma_i32_16x16x64_i8 v[26:29], v[180:183], v[216:219], v[26:29]
	v_mfma_i32_16x16x64_i8 v[18:21], v[188:191], v[216:219], v[18:21]
	v_mfma_i32_16x16x64_i8 v[14:17], v[180:183], v[224:227], v[14:17]
	v_mfma_i32_16x16x64_i8 v[10:13], v[188:191], v[224:227], v[10:13]
	s_setprio 0
	s_add_i32 s62, s62, 2
	s_cmp_gt_u32 s62, 13
	s_mov_b64 s[28:29], s[30:31]
	s_barrier
	s_cbranch_scc0 .LBB0_1154
	s_and_b64 vcc, exec, s[14:15]
	s_cbranch_vccz .LBB0_1157
	s_barrier

.LBB0_1237:
	ds_read_b128 v[18:21], v193
	ds_read_b128 v[22:25], v193 offset:1024
	ds_read_b128 v[26:29], v193 offset:2048
	ds_read_b128 v[30:33], v193 offset:3072
	ds_read_b128 v[2:5], v195
	ds_read_b128 v[6:9], v195 offset:1024
	ds_read_b128 v[10:13], v195 offset:2048
	ds_read_b128 v[14:17], v195 offset:3072
	s_add_u32 s26, s30, 0x100
	s_addc_u32 s27, s31, 0
	s_add_u32 s28, s56, s30
	s_addc_u32 s29, s57, s31
	s_add_i32 s68, s43, s34
	s_add_i32 m0, s35, 0xc000
	s_add_i32 s69, s35, 0xe000
	s_add_i32 s63, s68, 0x2000
	s_cmp_eq_u32 s62, 40
	s_cselect_b32 s29, s23, s29
	s_cselect_b32 s28, s22, s28
	s_cselect_b32 s66, 0, s27
	s_cselect_b32 s67, 0, s26
	v_lshl_add_u64 v[222:223], v[178:179], 0, s[30:31]
	ds_read_b128 v[182:185], v196
	ds_read_b128 v[186:189], v196 offset:1024
	ds_read_b128 v[198:201], v196 offset:2048
	ds_read_b128 v[202:205], v196 offset:3072
	ds_read_b128 v[206:209], v196 offset:4096
	ds_read_b128 v[210:213], v196 offset:5120
	ds_read_b128 v[214:217], v196 offset:6144
	ds_read_b128 v[218:221], v196 offset:7168
	global_load_lds_dwordx4 v[222:223], off
	v_lshl_add_u64 v[222:223], v[180:181], 0, s[30:31]
	s_mov_b32 m0, s69
	s_nop 0
	global_load_lds_dwordx4 v[222:223], off
	s_waitcnt vmcnt(8)
	s_waitcnt lgkmcnt(0)
	s_barrier
	s_setprio 1
	s_waitcnt lgkmcnt(0)
	v_mfma_scale_f32_16x16x128_f8f6f4 v[158:161], v[18:25], v[182:189], v[158:161], v190, v190 op_sel_hi:[0,0,0]
	v_mfma_scale_f32_16x16x128_f8f6f4 v[154:157], v[26:33], v[182:189], v[154:157], v190, v190 op_sel_hi:[0,0,0]
	v_mfma_scale_f32_16x16x128_f8f6f4 v[150:153], v[18:25], v[198:205], v[150:153], v190, v190 op_sel_hi:[0,0,0]
	v_mfma_scale_f32_16x16x128_f8f6f4 v[142:145], v[26:33], v[198:205], v[142:145], v190, v190 op_sel_hi:[0,0,0]
	v_mfma_scale_f32_16x16x128_f8f6f4 v[134:137], v[18:25], v[206:213], v[134:137], v190, v190 op_sel_hi:[0,0,0]
	v_mfma_scale_f32_16x16x128_f8f6f4 v[126:129], v[26:33], v[206:213], v[126:129], v190, v190 op_sel_hi:[0,0,0]
	v_mfma_scale_f32_16x16x128_f8f6f4 v[118:121], v[18:25], v[214:221], v[118:121], v190, v190 op_sel_hi:[0,0,0]
	v_mfma_scale_f32_16x16x128_f8f6f4 v[110:113], v[26:33], v[214:221], v[110:113], v190, v190 op_sel_hi:[0,0,0]
	s_setprio 0
	s_setprio 1
	v_mfma_scale_f32_16x16x128_f8f6f4 v[146:149], v[2:9], v[182:189], v[146:149], v190, v190 op_sel_hi:[0,0,0]
	v_mfma_scale_f32_16x16x128_f8f6f4 v[138:141], v[10:17], v[182:189], v[138:141], v190, v190 op_sel_hi:[0,0,0]
	v_mfma_scale_f32_16x16x128_f8f6f4 v[130:133], v[2:9], v[198:205], v[130:133], v190, v190 op_sel_hi:[0,0,0]
	v_mfma_scale_f32_16x16x128_f8f6f4 v[122:125], v[10:17], v[198:205], v[122:125], v190, v190 op_sel_hi:[0,0,0]
	v_mfma_scale_f32_16x16x128_f8f6f4 v[114:117], v[2:9], v[206:213], v[114:117], v190, v190 op_sel_hi:[0,0,0]
	v_mfma_scale_f32_16x16x128_f8f6f4 v[106:109], v[10:17], v[206:213], v[106:109], v190, v190 op_sel_hi:[0,0,0]
	v_mfma_scale_f32_16x16x128_f8f6f4 v[102:105], v[2:9], v[214:221], v[102:105], v190, v190 op_sel_hi:[0,0,0]
	v_mfma_scale_f32_16x16x128_f8f6f4 v[98:101], v[10:17], v[214:221], v[98:101], v190, v190 op_sel_hi:[0,0,0]
	s_setprio 0
	s_mov_b32 m0, s68
	v_lshl_add_u64 v[184:185], s[28:29], 0, v[162:163]
	s_barrier
	ds_read_b128 v[198:201], v196 offset:16384
	ds_read_b128 v[202:205], v196 offset:17408
	ds_read_b128 v[206:209], v196 offset:18432
	ds_read_b128 v[210:213], v196 offset:19456
	ds_read_b128 v[214:217], v196 offset:20480
	ds_read_b128 v[218:221], v196 offset:21504
	ds_read_b128 v[222:225], v196 offset:22528
	ds_read_b128 v[226:229], v196 offset:23552
	global_load_lds_dwordx4 v[184:185], off
	s_mov_b32 m0, s63
	s_cselect_b32 s63, s9, s25
	s_cselect_b32 s68, s8, s24
	s_add_u32 s30, s28, 0xb0000
	v_lshl_add_u64 v[182:183], s[28:29], 0, v[164:165]
	s_addc_u32 s31, s29, 0
	s_add_i32 s69, s44, s34
	global_load_lds_dwordx4 v[182:183], off
	v_lshl_add_u64 v[186:187], s[30:31], 0, v[162:163]
	s_mov_b32 m0, s69
	s_nop 0
	global_load_lds_dwordx4 v[186:187], off
	s_add_i32 m0, s69, 0x2000
	v_lshl_add_u64 v[186:187], s[30:31], 0, v[164:165]
	s_add_u32 s30, s68, s67
	s_addc_u32 s31, s63, s66
	global_load_lds_dwordx4 v[186:187], off
	v_lshl_add_u64 v[186:187], s[30:31], 0, v[166:167]
	s_mov_b32 m0, s35
	v_lshl_add_u64 v[188:189], s[30:31], 0, v[168:169]
	global_load_lds_dwordx4 v[186:187], off
	s_mov_b32 m0, s36
	s_nop 0
	global_load_lds_dwordx4 v[188:189], off
	s_waitcnt vmcnt(8)
	s_waitcnt lgkmcnt(0)
	s_barrier
	s_setprio 1
	s_waitcnt lgkmcnt(0)
	v_mfma_scale_f32_16x16x128_f8f6f4 v[94:97], v[18:25], v[198:205], v[94:97], v190, v190 op_sel_hi:[0,0,0]
	v_mfma_scale_f32_16x16x128_f8f6f4 v[90:93], v[26:33], v[198:205], v[90:93], v190, v190 op_sel_hi:[0,0,0]
	v_mfma_scale_f32_16x16x128_f8f6f4 v[86:89], v[18:25], v[206:213], v[86:89], v190, v190 op_sel_hi:[0,0,0]
	v_mfma_scale_f32_16x16x128_f8f6f4 v[78:81], v[26:33], v[206:213], v[78:81], v190, v190 op_sel_hi:[0,0,0]
	v_mfma_scale_f32_16x16x128_f8f6f4 v[62:65], v[18:25], v[214:221], v[62:65], v190, v190 op_sel_hi:[0,0,0]
	v_mfma_scale_f32_16x16x128_f8f6f4 v[54:57], v[26:33], v[214:221], v[54:57], v190, v190 op_sel_hi:[0,0,0]
	v_mfma_scale_f32_16x16x128_f8f6f4 v[46:49], v[18:25], v[222:229], v[46:49], v190, v190 op_sel_hi:[0,0,0]
	v_mfma_scale_f32_16x16x128_f8f6f4 v[38:41], v[26:33], v[222:229], v[38:41], v190, v190 op_sel_hi:[0,0,0]
	s_setprio 0
	s_setprio 1
	v_mfma_scale_f32_16x16x128_f8f6f4 v[82:85], v[2:9], v[198:205], v[82:85], v190, v190 op_sel_hi:[0,0,0]
	v_mfma_scale_f32_16x16x128_f8f6f4 v[74:77], v[10:17], v[198:205], v[74:77], v190, v190 op_sel_hi:[0,0,0]
	v_mfma_scale_f32_16x16x128_f8f6f4 v[58:61], v[2:9], v[206:213], v[58:61], v190, v190 op_sel_hi:[0,0,0]
	v_mfma_scale_f32_16x16x128_f8f6f4 v[50:53], v[10:17], v[206:213], v[50:53], v190, v190 op_sel_hi:[0,0,0]
	v_mfma_scale_f32_16x16x128_f8f6f4 v[42:45], v[2:9], v[214:221], v[42:45], v190, v190 op_sel_hi:[0,0,0]
	v_mfma_scale_f32_16x16x128_f8f6f4 v[34:37], v[10:17], v[214:221], v[34:37], v190, v190 op_sel_hi:[0,0,0]
	v_mfma_scale_f32_16x16x128_f8f6f4 v[70:73], v[2:9], v[222:229], v[70:73], v190, v190 op_sel_hi:[0,0,0]
	v_mfma_scale_f32_16x16x128_f8f6f4 v[66:69], v[10:17], v[222:229], v[66:69], v190, v190 op_sel_hi:[0,0,0]
	s_setprio 0
	s_add_i32 s63, 0, 0x18000
	s_add_i32 s66, 0, 0x1c000
	v_add_u32_e32 v14, s63, v191
	v_add_u32_e32 v30, s66, v191
	s_barrier
	ds_read_b128 v[2:5], v14
	ds_read_b128 v[6:9], v14 offset:1024
	ds_read_b128 v[10:13], v14 offset:2048
	ds_read_b128 v[14:17], v14 offset:3072
	ds_read_b128 v[18:21], v30
	ds_read_b128 v[22:25], v30 offset:1024
	ds_read_b128 v[26:29], v30 offset:2048
	ds_read_b128 v[30:33], v30 offset:3072
	s_add_u32 s30, s30, 0xb0000
	s_addc_u32 s31, s31, 0
	s_mov_b32 m0, s37
	v_lshl_add_u64 v[230:231], s[30:31], 0, v[166:167]
	ds_read_b128 v[198:201], v196 offset:32768
	ds_read_b128 v[202:205], v196 offset:33792
	ds_read_b128 v[206:209], v196 offset:34816
	ds_read_b128 v[210:213], v196 offset:35840
	ds_read_b128 v[214:217], v196 offset:36864
	ds_read_b128 v[218:221], v196 offset:37888
	ds_read_b128 v[222:225], v196 offset:38912
	ds_read_b128 v[226:229], v196 offset:39936
	global_load_lds_dwordx4 v[230:231], off
	v_lshl_add_u64 v[230:231], s[30:31], 0, v[168:169]
	s_mov_b32 m0, s38
	s_nop 0
	global_load_lds_dwordx4 v[230:231], off
	s_waitcnt vmcnt(8)
	s_waitcnt lgkmcnt(0)
	s_barrier
	s_setprio 1
	s_waitcnt lgkmcnt(0)
	v_mfma_scale_f32_16x16x128_f8f6f4 v[158:161], v[2:9], v[198:205], v[158:161], v190, v190 op_sel_hi:[0,0,0]
	v_mfma_scale_f32_16x16x128_f8f6f4 v[154:157], v[10:17], v[198:205], v[154:157], v190, v190 op_sel_hi:[0,0,0]
	v_mfma_scale_f32_16x16x128_f8f6f4 v[150:153], v[2:9], v[206:213], v[150:153], v190, v190 op_sel_hi:[0,0,0]
	v_mfma_scale_f32_16x16x128_f8f6f4 v[142:145], v[10:17], v[206:213], v[142:145], v190, v190 op_sel_hi:[0,0,0]
	v_mfma_scale_f32_16x16x128_f8f6f4 v[134:137], v[2:9], v[214:221], v[134:137], v190, v190 op_sel_hi:[0,0,0]
	v_mfma_scale_f32_16x16x128_f8f6f4 v[126:129], v[10:17], v[214:221], v[126:129], v190, v190 op_sel_hi:[0,0,0]
	v_mfma_scale_f32_16x16x128_f8f6f4 v[118:121], v[2:9], v[222:229], v[118:121], v190, v190 op_sel_hi:[0,0,0]
	v_mfma_scale_f32_16x16x128_f8f6f4 v[110:113], v[10:17], v[222:229], v[110:113], v190, v190 op_sel_hi:[0,0,0]
	s_setprio 0
	s_setprio 1
	v_mfma_scale_f32_16x16x128_f8f6f4 v[146:149], v[18:25], v[198:205], v[146:149], v190, v190 op_sel_hi:[0,0,0]
	v_mfma_scale_f32_16x16x128_f8f6f4 v[138:141], v[26:33], v[198:205], v[138:141], v190, v190 op_sel_hi:[0,0,0]
	v_mfma_scale_f32_16x16x128_f8f6f4 v[130:133], v[18:25], v[206:213], v[130:133], v190, v190 op_sel_hi:[0,0,0]
	v_mfma_scale_f32_16x16x128_f8f6f4 v[122:125], v[26:33], v[206:213], v[122:125], v190, v190 op_sel_hi:[0,0,0]
	v_mfma_scale_f32_16x16x128_f8f6f4 v[114:117], v[18:25], v[214:221], v[114:117], v190, v190 op_sel_hi:[0,0,0]
	v_mfma_scale_f32_16x16x128_f8f6f4 v[106:109], v[26:33], v[214:221], v[106:109], v190, v190 op_sel_hi:[0,0,0]
	v_mfma_scale_f32_16x16x128_f8f6f4 v[102:105], v[18:25], v[222:229], v[102:105], v190, v190 op_sel_hi:[0,0,0]
	v_mfma_scale_f32_16x16x128_f8f6f4 v[98:101], v[26:33], v[222:229], v[98:101], v190, v190 op_sel_hi:[0,0,0]
	s_setprio 0
	s_add_i32 s30, s63, s34
	v_lshl_add_u64 v[184:185], v[184:185], 0, s[12:13]
	s_mov_b32 m0, s30
	s_barrier
	ds_read_b128 v[198:201], v196 offset:49152
	ds_read_b128 v[202:205], v196 offset:50176
	ds_read_b128 v[206:209], v196 offset:51200
	ds_read_b128 v[210:213], v196 offset:52224
	ds_read_b128 v[214:217], v196 offset:53248
	ds_read_b128 v[218:221], v196 offset:54272
	ds_read_b128 v[222:225], v196 offset:55296
	ds_read_b128 v[226:229], v196 offset:56320
	global_load_lds_dwordx4 v[184:185], off
	s_add_i32 m0, s30, 0x2000
	s_add_u32 s28, s28, 0xb0080
	v_lshl_add_u64 v[182:183], v[182:183], 0, s[12:13]
	s_addc_u32 s29, s29, 0
	s_add_i32 s30, s66, s34
	global_load_lds_dwordx4 v[182:183], off
	v_lshl_add_u64 v[182:183], s[28:29], 0, v[162:163]
	s_mov_b32 m0, s30
	s_nop 0
	global_load_lds_dwordx4 v[182:183], off
	v_lshl_add_u64 v[182:183], s[28:29], 0, v[164:165]
	s_add_i32 m0, s30, 0x2000
	s_nop 0
	global_load_lds_dwordx4 v[182:183], off
	v_lshl_add_u64 v[182:183], v[186:187], 0, s[12:13]
	s_mov_b32 m0, s40
	s_nop 0
	global_load_lds_dwordx4 v[182:183], off
	v_lshl_add_u64 v[182:183], v[188:189], 0, s[12:13]
	s_mov_b32 m0, s41
	s_nop 0
	global_load_lds_dwordx4 v[182:183], off
	s_waitcnt vmcnt(8)
	s_waitcnt lgkmcnt(0)
	s_barrier
	s_setprio 1
	s_waitcnt lgkmcnt(0)
	v_mfma_scale_f32_16x16x128_f8f6f4 v[94:97], v[2:9], v[198:205], v[94:97], v190, v190 op_sel_hi:[0,0,0]
	v_mfma_scale_f32_16x16x128_f8f6f4 v[90:93], v[10:17], v[198:205], v[90:93], v190, v190 op_sel_hi:[0,0,0]
	v_mfma_scale_f32_16x16x128_f8f6f4 v[86:89], v[2:9], v[206:213], v[86:89], v190, v190 op_sel_hi:[0,0,0]
	v_mfma_scale_f32_16x16x128_f8f6f4 v[78:81], v[10:17], v[206:213], v[78:81], v190, v190 op_sel_hi:[0,0,0]
	v_mfma_scale_f32_16x16x128_f8f6f4 v[62:65], v[2:9], v[214:221], v[62:65], v190, v190 op_sel_hi:[0,0,0]
	v_mfma_scale_f32_16x16x128_f8f6f4 v[54:57], v[10:17], v[214:221], v[54:57], v190, v190 op_sel_hi:[0,0,0]
	v_mfma_scale_f32_16x16x128_f8f6f4 v[46:49], v[2:9], v[222:229], v[46:49], v190, v190 op_sel_hi:[0,0,0]
	v_mfma_scale_f32_16x16x128_f8f6f4 v[38:41], v[10:17], v[222:229], v[38:41], v190, v190 op_sel_hi:[0,0,0]
	s_setprio 0
	s_setprio 1
	v_mfma_scale_f32_16x16x128_f8f6f4 v[82:85], v[18:25], v[198:205], v[82:85], v190, v190 op_sel_hi:[0,0,0]
	v_mfma_scale_f32_16x16x128_f8f6f4 v[74:77], v[26:33], v[198:205], v[74:77], v190, v190 op_sel_hi:[0,0,0]
	v_mfma_scale_f32_16x16x128_f8f6f4 v[58:61], v[18:25], v[206:213], v[58:61], v190, v190 op_sel_hi:[0,0,0]
	v_mfma_scale_f32_16x16x128_f8f6f4 v[50:53], v[26:33], v[206:213], v[50:53], v190, v190 op_sel_hi:[0,0,0]
	v_mfma_scale_f32_16x16x128_f8f6f4 v[42:45], v[18:25], v[214:221], v[42:45], v190, v190 op_sel_hi:[0,0,0]
	v_mfma_scale_f32_16x16x128_f8f6f4 v[34:37], v[26:33], v[214:221], v[34:37], v190, v190 op_sel_hi:[0,0,0]
	v_mfma_scale_f32_16x16x128_f8f6f4 v[70:73], v[18:25], v[222:229], v[70:73], v190, v190 op_sel_hi:[0,0,0]
	v_mfma_scale_f32_16x16x128_f8f6f4 v[66:69], v[26:33], v[222:229], v[66:69], v190, v190 op_sel_hi:[0,0,0]
	s_setprio 0
	s_add_i32 s62, s62, 2
	s_cmp_gt_u32 s62, 41
	s_mov_b64 s[30:31], s[26:27]
	s_barrier
	s_cbranch_scc0 .LBB0_1237
	s_and_b64 vcc, exec, s[14:15]
	s_cbranch_vccz .LBB0_1240
	s_barrier

.LBB0_1385:
	ds_read_b128 v[152:155], v174
	ds_read_b128 v[156:159], v174 offset:1024
	ds_read_b128 v[160:163], v174 offset:2048
	ds_read_b128 v[164:167], v174 offset:3072
	ds_read_b128 v[168:171], v175
	ds_read_b128 v[180:183], v175 offset:1024
	ds_read_b128 v[184:187], v175 offset:2048
	ds_read_b128 v[188:191], v175 offset:3072
	s_add_u32 s38, s36, 0x100
	s_addc_u32 s39, s37, 0
	s_add_u32 s74, s25, s36
	s_addc_u32 s75, s70, s37
	s_cmp_eq_u32 s71, 12
	s_cselect_b64 s[42:43], -1, 0
	s_and_b64 s[40:41], s[42:43], exec
	s_cselect_b32 s76, 0, s38
	s_cselect_b32 s41, s0, s75
	s_cselect_b32 s40, s23, s74
	v_lshl_add_u64 v[192:193], v[148:149], 0, s[36:37]
	s_add_i32 m0, s47, 0xc000
	ds_read_b128 v[196:199], v176
	ds_read_b128 v[200:203], v176 offset:1024
	ds_read_b128 v[204:207], v176 offset:2048
	ds_read_b128 v[208:211], v176 offset:3072
	ds_read_b128 v[212:215], v176 offset:4096
	ds_read_b128 v[216:219], v176 offset:5120
	ds_read_b128 v[220:223], v176 offset:6144
	ds_read_b128 v[224:227], v176 offset:7168
	global_load_lds_dwordx4 v[192:193], off
	v_lshl_add_u64 v[192:193], v[150:151], 0, s[36:37]
	s_add_i32 m0, s47, 0xe000
	s_nop 0
	global_load_lds_dwordx4 v[192:193], off
	s_waitcnt vmcnt(8)
	s_waitcnt lgkmcnt(0)
	s_barrier
	s_setprio 1
	s_waitcnt lgkmcnt(0)
	v_mfma_i32_16x16x64_i8 v[126:129], v[152:155], v[196:199], v[126:129]
	v_mfma_i32_16x16x64_i8 v[122:125], v[160:163], v[196:199], v[122:125]
	v_mfma_i32_16x16x64_i8 v[110:113], v[152:155], v[204:207], v[110:113]
	v_mfma_i32_16x16x64_i8 v[106:109], v[160:163], v[204:207], v[106:109]
	v_mfma_i32_16x16x64_i8 v[94:97], v[152:155], v[212:215], v[94:97]
	v_mfma_i32_16x16x64_i8 v[90:93], v[160:163], v[212:215], v[90:93]
	v_mfma_i32_16x16x64_i8 v[78:81], v[152:155], v[220:223], v[78:81]
	v_mfma_i32_16x16x64_i8 v[74:77], v[160:163], v[220:223], v[74:77]
	v_mfma_i32_16x16x64_i8 v[126:129], v[156:159], v[200:203], v[126:129]
	v_mfma_i32_16x16x64_i8 v[122:125], v[164:167], v[200:203], v[122:125]
	v_mfma_i32_16x16x64_i8 v[110:113], v[156:159], v[208:211], v[110:113]
	v_mfma_i32_16x16x64_i8 v[106:109], v[164:167], v[208:211], v[106:109]
	v_mfma_i32_16x16x64_i8 v[94:97], v[156:159], v[216:219], v[94:97]
	v_mfma_i32_16x16x64_i8 v[90:93], v[164:167], v[216:219], v[90:93]
	v_mfma_i32_16x16x64_i8 v[78:81], v[156:159], v[224:227], v[78:81]
	v_mfma_i32_16x16x64_i8 v[74:77], v[164:167], v[224:227], v[74:77]
	s_setprio 0
	s_setprio 1
	v_mfma_i32_16x16x64_i8 v[118:121], v[168:171], v[196:199], v[118:121]
	v_mfma_i32_16x16x64_i8 v[114:117], v[184:187], v[196:199], v[114:117]
	v_mfma_i32_16x16x64_i8 v[102:105], v[168:171], v[204:207], v[102:105]
	v_mfma_i32_16x16x64_i8 v[98:101], v[184:187], v[204:207], v[98:101]
	v_mfma_i32_16x16x64_i8 v[86:89], v[168:171], v[212:215], v[86:89]
	v_mfma_i32_16x16x64_i8 v[82:85], v[184:187], v[212:215], v[82:85]
	v_mfma_i32_16x16x64_i8 v[70:73], v[168:171], v[220:223], v[70:73]
	v_mfma_i32_16x16x64_i8 v[66:69], v[184:187], v[220:223], v[66:69]
	v_mfma_i32_16x16x64_i8 v[118:121], v[180:183], v[200:203], v[118:121]
	v_mfma_i32_16x16x64_i8 v[114:117], v[188:191], v[200:203], v[114:117]
	v_mfma_i32_16x16x64_i8 v[102:105], v[180:183], v[208:211], v[102:105]
	v_mfma_i32_16x16x64_i8 v[98:101], v[188:191], v[208:211], v[98:101]
	v_mfma_i32_16x16x64_i8 v[86:89], v[180:183], v[216:219], v[86:89]
	v_mfma_i32_16x16x64_i8 v[82:85], v[188:191], v[216:219], v[82:85]
	v_mfma_i32_16x16x64_i8 v[70:73], v[180:183], v[224:227], v[70:73]
	v_mfma_i32_16x16x64_i8 v[66:69], v[188:191], v[224:227], v[66:69]
	s_setprio 0
	s_add_i32 s36, s66, s44
	v_lshl_add_u64 v[192:193], s[40:41], 0, v[134:135]
	s_mov_b32 m0, s36
	s_barrier
	ds_read_b128 v[196:199], v176 offset:16384
	ds_read_b128 v[200:203], v176 offset:17408
	ds_read_b128 v[204:207], v176 offset:18432
	ds_read_b128 v[208:211], v176 offset:19456
	ds_read_b128 v[212:215], v176 offset:20480
	ds_read_b128 v[216:219], v176 offset:21504
	ds_read_b128 v[220:223], v176 offset:22528
	ds_read_b128 v[224:227], v176 offset:23552
	global_load_lds_dwordx4 v[192:193], off
	s_add_i32 m0, s36, 0x2000
	s_add_u32 s36, s40, 0x40000
	v_lshl_add_u64 v[228:229], s[40:41], 0, v[132:133]
	s_addc_u32 s37, s41, 0
	s_add_i32 s74, s67, s44
	global_load_lds_dwordx4 v[228:229], off
	v_lshl_add_u64 v[230:231], s[36:37], 0, v[134:135]
	s_mov_b32 m0, s74
	s_nop 0
	global_load_lds_dwordx4 v[230:231], off
	v_lshl_add_u64 v[230:231], s[36:37], 0, v[132:133]
	s_add_i32 m0, s74, 0x2000
	s_and_b64 s[36:37], s[8:9], s[42:43]
	s_and_b64 s[36:37], s[36:37], exec
	s_cselect_b32 s36, s26, s34
	s_cselect_b32 s37, s27, s35
	s_add_u32 s36, s36, s76
	s_addc_u32 s37, s37, 0
	global_load_lds_dwordx4 v[230:231], off
	v_lshl_add_u64 v[230:231], s[36:37], 0, v[136:137]
	s_mov_b32 m0, s47
	v_lshl_add_u64 v[232:233], s[36:37], 0, v[138:139]
	global_load_lds_dwordx4 v[230:231], off
	s_mov_b32 m0, s49
	s_nop 0
	global_load_lds_dwordx4 v[232:233], off
	s_waitcnt vmcnt(8)
	s_waitcnt lgkmcnt(0)
	s_barrier
	s_setprio 1
	s_waitcnt lgkmcnt(0)
	v_mfma_i32_16x16x64_i8 v[62:65], v[152:155], v[196:199], v[62:65]
	v_mfma_i32_16x16x64_i8 v[58:61], v[160:163], v[196:199], v[58:61]
	v_mfma_i32_16x16x64_i8 v[46:49], v[152:155], v[204:207], v[46:49]
	v_mfma_i32_16x16x64_i8 v[42:45], v[160:163], v[204:207], v[42:45]
	v_mfma_i32_16x16x64_i8 v[30:33], v[152:155], v[212:215], v[30:33]
	v_mfma_i32_16x16x64_i8 v[26:29], v[160:163], v[212:215], v[26:29]
	v_mfma_i32_16x16x64_i8 v[6:9], v[152:155], v[220:223], v[6:9]
	v_mfma_i32_16x16x64_i8 v[2:5], v[160:163], v[220:223], v[2:5]
	v_mfma_i32_16x16x64_i8 v[62:65], v[156:159], v[200:203], v[62:65]
	v_mfma_i32_16x16x64_i8 v[58:61], v[164:167], v[200:203], v[58:61]
	v_mfma_i32_16x16x64_i8 v[46:49], v[156:159], v[208:211], v[46:49]
	v_mfma_i32_16x16x64_i8 v[42:45], v[164:167], v[208:211], v[42:45]
	v_mfma_i32_16x16x64_i8 v[30:33], v[156:159], v[216:219], v[30:33]
	v_mfma_i32_16x16x64_i8 v[26:29], v[164:167], v[216:219], v[26:29]
	v_mfma_i32_16x16x64_i8 v[6:9], v[156:159], v[224:227], v[6:9]
	v_mfma_i32_16x16x64_i8 v[2:5], v[164:167], v[224:227], v[2:5]
	s_setprio 0
	s_setprio 1
	v_mfma_i32_16x16x64_i8 v[54:57], v[168:171], v[196:199], v[54:57]
	v_mfma_i32_16x16x64_i8 v[50:53], v[184:187], v[196:199], v[50:53]
	v_mfma_i32_16x16x64_i8 v[38:41], v[168:171], v[204:207], v[38:41]
	v_mfma_i32_16x16x64_i8 v[34:37], v[184:187], v[204:207], v[34:37]
	v_mfma_i32_16x16x64_i8 v[14:17], v[168:171], v[212:215], v[14:17]
	v_mfma_i32_16x16x64_i8 v[10:13], v[184:187], v[212:215], v[10:13]
	v_mfma_i32_16x16x64_i8 v[22:25], v[168:171], v[220:223], v[22:25]
	v_mfma_i32_16x16x64_i8 v[18:21], v[184:187], v[220:223], v[18:21]
	v_mfma_i32_16x16x64_i8 v[54:57], v[180:183], v[200:203], v[54:57]
	v_mfma_i32_16x16x64_i8 v[50:53], v[188:191], v[200:203], v[50:53]
	v_mfma_i32_16x16x64_i8 v[38:41], v[180:183], v[208:211], v[38:41]
	v_mfma_i32_16x16x64_i8 v[34:37], v[188:191], v[208:211], v[34:37]
	v_mfma_i32_16x16x64_i8 v[14:17], v[180:183], v[216:219], v[14:17]
	v_mfma_i32_16x16x64_i8 v[10:13], v[188:191], v[216:219], v[10:13]
	v_mfma_i32_16x16x64_i8 v[22:25], v[180:183], v[224:227], v[22:25]
	v_mfma_i32_16x16x64_i8 v[18:21], v[188:191], v[224:227], v[18:21]
	s_setprio 0
	s_add_i32 s42, 0, 0x18000
	v_add_u32_e32 v1, s42, v172
	s_add_i32 s43, 0, 0x1c000
	s_barrier
	ds_read_b128 v[152:155], v1
	ds_read_b128 v[156:159], v1 offset:1024
	ds_read_b128 v[160:163], v1 offset:2048
	ds_read_b128 v[164:167], v1 offset:3072
	v_add_u32_e32 v1, s43, v172
	ds_read_b128 v[168:171], v1
	ds_read_b128 v[180:183], v1 offset:1024
	ds_read_b128 v[184:187], v1 offset:2048
	ds_read_b128 v[188:191], v1 offset:3072
	s_add_u32 s36, s36, 0x40000
	s_addc_u32 s37, s37, 0
	s_mov_b32 m0, s52
	v_lshl_add_u64 v[234:235], s[36:37], 0, v[136:137]
	ds_read_b128 v[196:199], v176 offset:32768
	ds_read_b128 v[200:203], v176 offset:33792
	ds_read_b128 v[204:207], v176 offset:34816
	ds_read_b128 v[208:211], v176 offset:35840
	ds_read_b128 v[212:215], v176 offset:36864
	ds_read_b128 v[216:219], v176 offset:37888
	ds_read_b128 v[220:223], v176 offset:38912
	ds_read_b128 v[224:227], v176 offset:39936
	global_load_lds_dwordx4 v[234:235], off
	v_lshl_add_u64 v[234:235], s[36:37], 0, v[138:139]
	s_mov_b32 m0, s53
	s_nop 0
	global_load_lds_dwordx4 v[234:235], off
	s_waitcnt vmcnt(8)
	s_waitcnt lgkmcnt(0)
	s_barrier
	s_setprio 1
	s_waitcnt lgkmcnt(0)
	v_mfma_i32_16x16x64_i8 v[126:129], v[152:155], v[196:199], v[126:129]
	v_mfma_i32_16x16x64_i8 v[122:125], v[160:163], v[196:199], v[122:125]
	v_mfma_i32_16x16x64_i8 v[110:113], v[152:155], v[204:207], v[110:113]
	v_mfma_i32_16x16x64_i8 v[106:109], v[160:163], v[204:207], v[106:109]
	v_mfma_i32_16x16x64_i8 v[94:97], v[152:155], v[212:215], v[94:97]
	v_mfma_i32_16x16x64_i8 v[90:93], v[160:163], v[212:215], v[90:93]
	v_mfma_i32_16x16x64_i8 v[78:81], v[152:155], v[220:223], v[78:81]
	v_mfma_i32_16x16x64_i8 v[74:77], v[160:163], v[220:223], v[74:77]
	v_mfma_i32_16x16x64_i8 v[126:129], v[156:159], v[200:203], v[126:129]
	v_mfma_i32_16x16x64_i8 v[122:125], v[164:167], v[200:203], v[122:125]
	v_mfma_i32_16x16x64_i8 v[110:113], v[156:159], v[208:211], v[110:113]
	v_mfma_i32_16x16x64_i8 v[106:109], v[164:167], v[208:211], v[106:109]
	v_mfma_i32_16x16x64_i8 v[94:97], v[156:159], v[216:219], v[94:97]
	v_mfma_i32_16x16x64_i8 v[90:93], v[164:167], v[216:219], v[90:93]
	v_mfma_i32_16x16x64_i8 v[78:81], v[156:159], v[224:227], v[78:81]
	v_mfma_i32_16x16x64_i8 v[74:77], v[164:167], v[224:227], v[74:77]
	s_setprio 0
	s_setprio 1
	v_mfma_i32_16x16x64_i8 v[118:121], v[168:171], v[196:199], v[118:121]
	v_mfma_i32_16x16x64_i8 v[114:117], v[184:187], v[196:199], v[114:117]
	v_mfma_i32_16x16x64_i8 v[102:105], v[168:171], v[204:207], v[102:105]
	v_mfma_i32_16x16x64_i8 v[98:101], v[184:187], v[204:207], v[98:101]
	v_mfma_i32_16x16x64_i8 v[86:89], v[168:171], v[212:215], v[86:89]
	v_mfma_i32_16x16x64_i8 v[82:85], v[184:187], v[212:215], v[82:85]
	v_mfma_i32_16x16x64_i8 v[70:73], v[168:171], v[220:223], v[70:73]
	v_mfma_i32_16x16x64_i8 v[66:69], v[184:187], v[220:223], v[66:69]
	v_mfma_i32_16x16x64_i8 v[118:121], v[180:183], v[200:203], v[118:121]
	v_mfma_i32_16x16x64_i8 v[114:117], v[188:191], v[200:203], v[114:117]
	v_mfma_i32_16x16x64_i8 v[102:105], v[180:183], v[208:211], v[102:105]
	v_mfma_i32_16x16x64_i8 v[98:101], v[188:191], v[208:211], v[98:101]
	v_mfma_i32_16x16x64_i8 v[86:89], v[180:183], v[216:219], v[86:89]
	v_mfma_i32_16x16x64_i8 v[82:85], v[188:191], v[216:219], v[82:85]
	v_mfma_i32_16x16x64_i8 v[70:73], v[180:183], v[224:227], v[70:73]
	v_mfma_i32_16x16x64_i8 v[66:69], v[188:191], v[224:227], v[66:69]
	s_setprio 0
	s_add_i32 s36, s42, s44
	v_lshl_add_u64 v[192:193], v[192:193], 0, s[18:19]
	s_mov_b32 m0, s36
	s_barrier
	ds_read_b128 v[196:199], v176 offset:49152
	ds_read_b128 v[200:203], v176 offset:50176
	ds_read_b128 v[204:207], v176 offset:51200
	ds_read_b128 v[208:211], v176 offset:52224
	ds_read_b128 v[212:215], v176 offset:53248
	ds_read_b128 v[216:219], v176 offset:54272
	ds_read_b128 v[220:223], v176 offset:55296
	ds_read_b128 v[224:227], v176 offset:56320
	global_load_lds_dwordx4 v[192:193], off
	s_add_i32 m0, s36, 0x2000
	s_add_u32 s36, s40, 0x40080
	v_lshl_add_u64 v[192:193], v[228:229], 0, s[18:19]
	s_addc_u32 s37, s41, 0
	s_add_i32 s40, s43, s44
	global_load_lds_dwordx4 v[192:193], off
	v_lshl_add_u64 v[192:193], s[36:37], 0, v[134:135]
	s_mov_b32 m0, s40
	s_nop 0
	global_load_lds_dwordx4 v[192:193], off
	v_lshl_add_u64 v[192:193], s[36:37], 0, v[132:133]
	s_add_i32 m0, s40, 0x2000
	s_nop 0
	global_load_lds_dwordx4 v[192:193], off
	v_lshl_add_u64 v[192:193], v[230:231], 0, s[18:19]
	s_mov_b32 m0, s57
	s_nop 0
	global_load_lds_dwordx4 v[192:193], off
	v_lshl_add_u64 v[192:193], v[232:233], 0, s[18:19]
	s_mov_b32 m0, s62
	s_nop 0
	global_load_lds_dwordx4 v[192:193], off
	s_waitcnt vmcnt(8)
	s_waitcnt lgkmcnt(0)
	s_barrier
	s_setprio 1
	s_waitcnt lgkmcnt(0)
	v_mfma_i32_16x16x64_i8 v[62:65], v[152:155], v[196:199], v[62:65]
	v_mfma_i32_16x16x64_i8 v[58:61], v[160:163], v[196:199], v[58:61]
	v_mfma_i32_16x16x64_i8 v[46:49], v[152:155], v[204:207], v[46:49]
	v_mfma_i32_16x16x64_i8 v[42:45], v[160:163], v[204:207], v[42:45]
	v_mfma_i32_16x16x64_i8 v[30:33], v[152:155], v[212:215], v[30:33]
	v_mfma_i32_16x16x64_i8 v[26:29], v[160:163], v[212:215], v[26:29]
	v_mfma_i32_16x16x64_i8 v[6:9], v[152:155], v[220:223], v[6:9]
	v_mfma_i32_16x16x64_i8 v[2:5], v[160:163], v[220:223], v[2:5]
	v_mfma_i32_16x16x64_i8 v[62:65], v[156:159], v[200:203], v[62:65]
	v_mfma_i32_16x16x64_i8 v[58:61], v[164:167], v[200:203], v[58:61]
	v_mfma_i32_16x16x64_i8 v[46:49], v[156:159], v[208:211], v[46:49]
	v_mfma_i32_16x16x64_i8 v[42:45], v[164:167], v[208:211], v[42:45]
	v_mfma_i32_16x16x64_i8 v[30:33], v[156:159], v[216:219], v[30:33]
	v_mfma_i32_16x16x64_i8 v[26:29], v[164:167], v[216:219], v[26:29]
	v_mfma_i32_16x16x64_i8 v[6:9], v[156:159], v[224:227], v[6:9]
	v_mfma_i32_16x16x64_i8 v[2:5], v[164:167], v[224:227], v[2:5]
	s_setprio 0
	s_setprio 1
	v_mfma_i32_16x16x64_i8 v[54:57], v[168:171], v[196:199], v[54:57]
	v_mfma_i32_16x16x64_i8 v[50:53], v[184:187], v[196:199], v[50:53]
	v_mfma_i32_16x16x64_i8 v[38:41], v[168:171], v[204:207], v[38:41]
	v_mfma_i32_16x16x64_i8 v[34:37], v[184:187], v[204:207], v[34:37]
	v_mfma_i32_16x16x64_i8 v[14:17], v[168:171], v[212:215], v[14:17]
	v_mfma_i32_16x16x64_i8 v[10:13], v[184:187], v[212:215], v[10:13]
	v_mfma_i32_16x16x64_i8 v[22:25], v[168:171], v[220:223], v[22:25]
	v_mfma_i32_16x16x64_i8 v[18:21], v[184:187], v[220:223], v[18:21]
	v_mfma_i32_16x16x64_i8 v[54:57], v[180:183], v[200:203], v[54:57]
	v_mfma_i32_16x16x64_i8 v[50:53], v[188:191], v[200:203], v[50:53]
	v_mfma_i32_16x16x64_i8 v[38:41], v[180:183], v[208:211], v[38:41]
	v_mfma_i32_16x16x64_i8 v[34:37], v[188:191], v[208:211], v[34:37]
	v_mfma_i32_16x16x64_i8 v[14:17], v[180:183], v[216:219], v[14:17]
	v_mfma_i32_16x16x64_i8 v[10:13], v[188:191], v[216:219], v[10:13]
	v_mfma_i32_16x16x64_i8 v[22:25], v[180:183], v[224:227], v[22:25]
	v_mfma_i32_16x16x64_i8 v[18:21], v[188:191], v[224:227], v[18:21]
	s_setprio 0
	s_add_i32 s71, s71, 2
	s_cmp_gt_u32 s71, 13
	s_mov_b64 s[36:37], s[38:39]
	s_barrier
	s_cbranch_scc0 .LBB0_1385
	s_and_b64 vcc, exec, s[20:21]
	s_cbranch_vccz .LBB0_1388
	s_barrier

.LBB0_2108:
	ds_read_b128 v[18:21], v193
	ds_read_b128 v[22:25], v193 offset:1024
	ds_read_b128 v[26:29], v193 offset:2048
	ds_read_b128 v[30:33], v193 offset:3072
	ds_read_b128 v[2:5], v195
	ds_read_b128 v[6:9], v195 offset:1024
	ds_read_b128 v[10:13], v195 offset:2048
	ds_read_b128 v[14:17], v195 offset:3072
	s_add_u32 s38, s42, 0x100
	s_addc_u32 s39, s43, 0
	s_add_u32 s71, s68, s42
	s_addc_u32 s74, s69, s43
	s_cmp_eq_u32 s70, 12
	s_cselect_b64 s[44:45], -1, 0
	s_and_b64 s[40:41], s[44:45], exec
	s_cselect_b32 s41, s25, s74
	s_cselect_b32 s40, s27, s71
	s_cselect_b32 s71, 0, s39
	s_cselect_b32 s74, 0, s38
	v_lshl_add_u64 v[222:223], v[178:179], 0, s[42:43]
	s_add_i32 m0, s35, 0xc000
	ds_read_b128 v[182:185], v196
	ds_read_b128 v[186:189], v196 offset:1024
	ds_read_b128 v[198:201], v196 offset:2048
	ds_read_b128 v[202:205], v196 offset:3072
	ds_read_b128 v[206:209], v196 offset:4096
	ds_read_b128 v[210:213], v196 offset:5120
	ds_read_b128 v[214:217], v196 offset:6144
	ds_read_b128 v[218:221], v196 offset:7168
	global_load_lds_dwordx4 v[222:223], off
	v_lshl_add_u64 v[222:223], v[180:181], 0, s[42:43]
	s_add_i32 m0, s35, 0xe000
	s_nop 0
	global_load_lds_dwordx4 v[222:223], off
	s_waitcnt vmcnt(8)
	s_waitcnt lgkmcnt(0)
	s_barrier
	s_setprio 1
	s_waitcnt lgkmcnt(0)
	v_mfma_scale_f32_16x16x128_f8f6f4 v[158:161], v[18:25], v[182:189], v[158:161], v1, v1 op_sel_hi:[0,0,0]
	v_mfma_scale_f32_16x16x128_f8f6f4 v[154:157], v[26:33], v[182:189], v[154:157], v1, v1 op_sel_hi:[0,0,0]
	v_mfma_scale_f32_16x16x128_f8f6f4 v[150:153], v[18:25], v[198:205], v[150:153], v1, v1 op_sel_hi:[0,0,0]
	v_mfma_scale_f32_16x16x128_f8f6f4 v[142:145], v[26:33], v[198:205], v[142:145], v1, v1 op_sel_hi:[0,0,0]
	v_mfma_scale_f32_16x16x128_f8f6f4 v[134:137], v[18:25], v[206:213], v[134:137], v1, v1 op_sel_hi:[0,0,0]
	v_mfma_scale_f32_16x16x128_f8f6f4 v[126:129], v[26:33], v[206:213], v[126:129], v1, v1 op_sel_hi:[0,0,0]
	v_mfma_scale_f32_16x16x128_f8f6f4 v[118:121], v[18:25], v[214:221], v[118:121], v1, v1 op_sel_hi:[0,0,0]
	v_mfma_scale_f32_16x16x128_f8f6f4 v[110:113], v[26:33], v[214:221], v[110:113], v1, v1 op_sel_hi:[0,0,0]
	s_setprio 0
	s_setprio 1
	v_mfma_scale_f32_16x16x128_f8f6f4 v[146:149], v[2:9], v[182:189], v[146:149], v1, v1 op_sel_hi:[0,0,0]
	v_mfma_scale_f32_16x16x128_f8f6f4 v[138:141], v[10:17], v[182:189], v[138:141], v1, v1 op_sel_hi:[0,0,0]
	v_mfma_scale_f32_16x16x128_f8f6f4 v[130:133], v[2:9], v[198:205], v[130:133], v1, v1 op_sel_hi:[0,0,0]
	v_mfma_scale_f32_16x16x128_f8f6f4 v[122:125], v[10:17], v[198:205], v[122:125], v1, v1 op_sel_hi:[0,0,0]
	v_mfma_scale_f32_16x16x128_f8f6f4 v[114:117], v[2:9], v[206:213], v[114:117], v1, v1 op_sel_hi:[0,0,0]
	v_mfma_scale_f32_16x16x128_f8f6f4 v[106:109], v[10:17], v[206:213], v[106:109], v1, v1 op_sel_hi:[0,0,0]
	v_mfma_scale_f32_16x16x128_f8f6f4 v[102:105], v[2:9], v[214:221], v[102:105], v1, v1 op_sel_hi:[0,0,0]
	v_mfma_scale_f32_16x16x128_f8f6f4 v[98:101], v[10:17], v[214:221], v[98:101], v1, v1 op_sel_hi:[0,0,0]
	s_setprio 0
	s_add_i32 s42, s57, s46
	v_lshl_add_u64 v[182:183], s[40:41], 0, v[162:163]
	s_mov_b32 m0, s42
	s_barrier
	ds_read_b128 v[198:201], v196 offset:16384
	ds_read_b128 v[202:205], v196 offset:17408
	ds_read_b128 v[206:209], v196 offset:18432
	ds_read_b128 v[210:213], v196 offset:19456
	ds_read_b128 v[214:217], v196 offset:20480
	ds_read_b128 v[218:221], v196 offset:21504
	ds_read_b128 v[222:225], v196 offset:22528
	ds_read_b128 v[226:229], v196 offset:23552
	global_load_lds_dwordx4 v[182:183], off
	s_add_i32 m0, s42, 0x2000
	s_add_u32 s42, s40, 0x40000
	v_lshl_add_u64 v[184:185], s[40:41], 0, v[164:165]
	s_addc_u32 s43, s41, 0
	s_add_i32 s75, s62, s46
	global_load_lds_dwordx4 v[184:185], off
	v_lshl_add_u64 v[186:187], s[42:43], 0, v[162:163]
	s_mov_b32 m0, s75
	s_nop 0
	global_load_lds_dwordx4 v[186:187], off
	v_lshl_add_u64 v[186:187], s[42:43], 0, v[164:165]
	s_add_i32 m0, s75, 0x2000
	s_and_b64 s[42:43], s[6:7], s[44:45]
	s_and_b64 s[42:43], s[42:43], exec
	s_cselect_b32 s42, s28, s36
	s_cselect_b32 s43, s29, s37
	s_add_u32 s42, s42, s74
	s_addc_u32 s43, s43, s71
	global_load_lds_dwordx4 v[186:187], off
	v_lshl_add_u64 v[186:187], s[42:43], 0, v[166:167]
	s_mov_b32 m0, s35
	v_lshl_add_u64 v[188:189], s[42:43], 0, v[168:169]
	global_load_lds_dwordx4 v[186:187], off
	s_mov_b32 m0, s47
	s_nop 0
	global_load_lds_dwordx4 v[188:189], off
	s_waitcnt vmcnt(8)
	s_waitcnt lgkmcnt(0)
	s_barrier
	s_setprio 1
	s_waitcnt lgkmcnt(0)
	v_mfma_scale_f32_16x16x128_f8f6f4 v[94:97], v[18:25], v[198:205], v[94:97], v1, v1 op_sel_hi:[0,0,0]
	v_mfma_scale_f32_16x16x128_f8f6f4 v[90:93], v[26:33], v[198:205], v[90:93], v1, v1 op_sel_hi:[0,0,0]
	v_mfma_scale_f32_16x16x128_f8f6f4 v[86:89], v[18:25], v[206:213], v[86:89], v1, v1 op_sel_hi:[0,0,0]
	v_mfma_scale_f32_16x16x128_f8f6f4 v[78:81], v[26:33], v[206:213], v[78:81], v1, v1 op_sel_hi:[0,0,0]
	v_mfma_scale_f32_16x16x128_f8f6f4 v[62:65], v[18:25], v[214:221], v[62:65], v1, v1 op_sel_hi:[0,0,0]
	v_mfma_scale_f32_16x16x128_f8f6f4 v[54:57], v[26:33], v[214:221], v[54:57], v1, v1 op_sel_hi:[0,0,0]
	v_mfma_scale_f32_16x16x128_f8f6f4 v[46:49], v[18:25], v[222:229], v[46:49], v1, v1 op_sel_hi:[0,0,0]
	v_mfma_scale_f32_16x16x128_f8f6f4 v[38:41], v[26:33], v[222:229], v[38:41], v1, v1 op_sel_hi:[0,0,0]
	s_setprio 0
	s_setprio 1
	v_mfma_scale_f32_16x16x128_f8f6f4 v[82:85], v[2:9], v[198:205], v[82:85], v1, v1 op_sel_hi:[0,0,0]
	v_mfma_scale_f32_16x16x128_f8f6f4 v[74:77], v[10:17], v[198:205], v[74:77], v1, v1 op_sel_hi:[0,0,0]
	v_mfma_scale_f32_16x16x128_f8f6f4 v[58:61], v[2:9], v[206:213], v[58:61], v1, v1 op_sel_hi:[0,0,0]
	v_mfma_scale_f32_16x16x128_f8f6f4 v[50:53], v[10:17], v[206:213], v[50:53], v1, v1 op_sel_hi:[0,0,0]
	v_mfma_scale_f32_16x16x128_f8f6f4 v[42:45], v[2:9], v[214:221], v[42:45], v1, v1 op_sel_hi:[0,0,0]
	v_mfma_scale_f32_16x16x128_f8f6f4 v[34:37], v[10:17], v[214:221], v[34:37], v1, v1 op_sel_hi:[0,0,0]
	v_mfma_scale_f32_16x16x128_f8f6f4 v[70:73], v[2:9], v[222:229], v[70:73], v1, v1 op_sel_hi:[0,0,0]
	v_mfma_scale_f32_16x16x128_f8f6f4 v[66:69], v[10:17], v[222:229], v[66:69], v1, v1 op_sel_hi:[0,0,0]
	s_setprio 0
	s_add_i32 s44, 0, 0x18000
	s_add_i32 s45, 0, 0x1c000
	v_add_u32_e32 v14, s44, v191
	v_add_u32_e32 v30, s45, v191
	s_barrier
	ds_read_b128 v[2:5], v14
	ds_read_b128 v[6:9], v14 offset:1024
	ds_read_b128 v[10:13], v14 offset:2048
	ds_read_b128 v[14:17], v14 offset:3072
	ds_read_b128 v[18:21], v30
	ds_read_b128 v[22:25], v30 offset:1024
	ds_read_b128 v[26:29], v30 offset:2048
	ds_read_b128 v[30:33], v30 offset:3072
	s_add_u32 s42, s42, 0x40000
	s_addc_u32 s43, s43, 0
	s_mov_b32 m0, s49
	v_lshl_add_u64 v[230:231], s[42:43], 0, v[166:167]
	ds_read_b128 v[198:201], v196 offset:32768
	ds_read_b128 v[202:205], v196 offset:33792
	ds_read_b128 v[206:209], v196 offset:34816
	ds_read_b128 v[210:213], v196 offset:35840
	ds_read_b128 v[214:217], v196 offset:36864
	ds_read_b128 v[218:221], v196 offset:37888
	ds_read_b128 v[222:225], v196 offset:38912
	ds_read_b128 v[226:229], v196 offset:39936
	global_load_lds_dwordx4 v[230:231], off
	v_lshl_add_u64 v[230:231], s[42:43], 0, v[168:169]
	s_mov_b32 m0, s52
	s_nop 0
	global_load_lds_dwordx4 v[230:231], off
	s_waitcnt vmcnt(8)
	s_waitcnt lgkmcnt(0)
	s_barrier
	s_setprio 1
	s_waitcnt lgkmcnt(0)
	v_mfma_scale_f32_16x16x128_f8f6f4 v[158:161], v[2:9], v[198:205], v[158:161], v1, v1 op_sel_hi:[0,0,0]
	v_mfma_scale_f32_16x16x128_f8f6f4 v[154:157], v[10:17], v[198:205], v[154:157], v1, v1 op_sel_hi:[0,0,0]
	v_mfma_scale_f32_16x16x128_f8f6f4 v[150:153], v[2:9], v[206:213], v[150:153], v1, v1 op_sel_hi:[0,0,0]
	v_mfma_scale_f32_16x16x128_f8f6f4 v[142:145], v[10:17], v[206:213], v[142:145], v1, v1 op_sel_hi:[0,0,0]
	v_mfma_scale_f32_16x16x128_f8f6f4 v[134:137], v[2:9], v[214:221], v[134:137], v1, v1 op_sel_hi:[0,0,0]
	v_mfma_scale_f32_16x16x128_f8f6f4 v[126:129], v[10:17], v[214:221], v[126:129], v1, v1 op_sel_hi:[0,0,0]
	v_mfma_scale_f32_16x16x128_f8f6f4 v[118:121], v[2:9], v[222:229], v[118:121], v1, v1 op_sel_hi:[0,0,0]
	v_mfma_scale_f32_16x16x128_f8f6f4 v[110:113], v[10:17], v[222:229], v[110:113], v1, v1 op_sel_hi:[0,0,0]
	s_setprio 0
	s_setprio 1
	v_mfma_scale_f32_16x16x128_f8f6f4 v[146:149], v[18:25], v[198:205], v[146:149], v1, v1 op_sel_hi:[0,0,0]
	v_mfma_scale_f32_16x16x128_f8f6f4 v[138:141], v[26:33], v[198:205], v[138:141], v1, v1 op_sel_hi:[0,0,0]
	v_mfma_scale_f32_16x16x128_f8f6f4 v[130:133], v[18:25], v[206:213], v[130:133], v1, v1 op_sel_hi:[0,0,0]
	v_mfma_scale_f32_16x16x128_f8f6f4 v[122:125], v[26:33], v[206:213], v[122:125], v1, v1 op_sel_hi:[0,0,0]
	v_mfma_scale_f32_16x16x128_f8f6f4 v[114:117], v[18:25], v[214:221], v[114:117], v1, v1 op_sel_hi:[0,0,0]
	v_mfma_scale_f32_16x16x128_f8f6f4 v[106:109], v[26:33], v[214:221], v[106:109], v1, v1 op_sel_hi:[0,0,0]
	v_mfma_scale_f32_16x16x128_f8f6f4 v[102:105], v[18:25], v[222:229], v[102:105], v1, v1 op_sel_hi:[0,0,0]
	v_mfma_scale_f32_16x16x128_f8f6f4 v[98:101], v[26:33], v[222:229], v[98:101], v1, v1 op_sel_hi:[0,0,0]
	s_setprio 0
	s_add_i32 s42, s44, s46
	v_lshl_add_u64 v[182:183], v[182:183], 0, s[10:11]
	s_mov_b32 m0, s42
	s_barrier
	ds_read_b128 v[198:201], v196 offset:49152
	ds_read_b128 v[202:205], v196 offset:50176
	ds_read_b128 v[206:209], v196 offset:51200
	ds_read_b128 v[210:213], v196 offset:52224
	ds_read_b128 v[214:217], v196 offset:53248
	ds_read_b128 v[218:221], v196 offset:54272
	ds_read_b128 v[222:225], v196 offset:55296
	ds_read_b128 v[226:229], v196 offset:56320
	global_load_lds_dwordx4 v[182:183], off
	s_add_i32 m0, s42, 0x2000
	s_add_u32 s40, s40, 0x40080
	v_lshl_add_u64 v[182:183], v[184:185], 0, s[10:11]
	s_addc_u32 s41, s41, 0
	s_add_i32 s42, s45, s46
	global_load_lds_dwordx4 v[182:183], off
	v_lshl_add_u64 v[182:183], s[40:41], 0, v[162:163]
	s_mov_b32 m0, s42
	s_nop 0
	global_load_lds_dwordx4 v[182:183], off
	v_lshl_add_u64 v[182:183], s[40:41], 0, v[164:165]
	s_add_i32 m0, s42, 0x2000
	s_nop 0
	global_load_lds_dwordx4 v[182:183], off
	v_lshl_add_u64 v[182:183], v[186:187], 0, s[10:11]
	s_mov_b32 m0, s54
	s_nop 0
	global_load_lds_dwordx4 v[182:183], off
	v_lshl_add_u64 v[182:183], v[188:189], 0, s[10:11]
	s_mov_b32 m0, s55
	s_nop 0
	global_load_lds_dwordx4 v[182:183], off
	s_waitcnt vmcnt(8)
	s_waitcnt lgkmcnt(0)
	s_barrier
	s_setprio 1
	s_waitcnt lgkmcnt(0)
	v_mfma_scale_f32_16x16x128_f8f6f4 v[94:97], v[2:9], v[198:205], v[94:97], v1, v1 op_sel_hi:[0,0,0]
	v_mfma_scale_f32_16x16x128_f8f6f4 v[90:93], v[10:17], v[198:205], v[90:93], v1, v1 op_sel_hi:[0,0,0]
	v_mfma_scale_f32_16x16x128_f8f6f4 v[86:89], v[2:9], v[206:213], v[86:89], v1, v1 op_sel_hi:[0,0,0]
	v_mfma_scale_f32_16x16x128_f8f6f4 v[78:81], v[10:17], v[206:213], v[78:81], v1, v1 op_sel_hi:[0,0,0]
	v_mfma_scale_f32_16x16x128_f8f6f4 v[62:65], v[2:9], v[214:221], v[62:65], v1, v1 op_sel_hi:[0,0,0]
	v_mfma_scale_f32_16x16x128_f8f6f4 v[54:57], v[10:17], v[214:221], v[54:57], v1, v1 op_sel_hi:[0,0,0]
	v_mfma_scale_f32_16x16x128_f8f6f4 v[46:49], v[2:9], v[222:229], v[46:49], v1, v1 op_sel_hi:[0,0,0]
	v_mfma_scale_f32_16x16x128_f8f6f4 v[38:41], v[10:17], v[222:229], v[38:41], v1, v1 op_sel_hi:[0,0,0]
	s_setprio 0
	s_setprio 1
	v_mfma_scale_f32_16x16x128_f8f6f4 v[82:85], v[18:25], v[198:205], v[82:85], v1, v1 op_sel_hi:[0,0,0]
	v_mfma_scale_f32_16x16x128_f8f6f4 v[74:77], v[26:33], v[198:205], v[74:77], v1, v1 op_sel_hi:[0,0,0]
	v_mfma_scale_f32_16x16x128_f8f6f4 v[58:61], v[18:25], v[206:213], v[58:61], v1, v1 op_sel_hi:[0,0,0]
	v_mfma_scale_f32_16x16x128_f8f6f4 v[50:53], v[26:33], v[206:213], v[50:53], v1, v1 op_sel_hi:[0,0,0]
	v_mfma_scale_f32_16x16x128_f8f6f4 v[42:45], v[18:25], v[214:221], v[42:45], v1, v1 op_sel_hi:[0,0,0]
	v_mfma_scale_f32_16x16x128_f8f6f4 v[34:37], v[26:33], v[214:221], v[34:37], v1, v1 op_sel_hi:[0,0,0]
	v_mfma_scale_f32_16x16x128_f8f6f4 v[70:73], v[18:25], v[222:229], v[70:73], v1, v1 op_sel_hi:[0,0,0]
	v_mfma_scale_f32_16x16x128_f8f6f4 v[66:69], v[26:33], v[222:229], v[66:69], v1, v1 op_sel_hi:[0,0,0]
	s_setprio 0
	s_add_i32 s70, s70, 2
	s_cmp_gt_u32 s70, 13
	s_mov_b64 s[42:43], s[38:39]
	s_barrier
	s_cbranch_scc0 .LBB0_2108
	s_and_b64 vcc, exec, s[12:13]
	s_cbranch_vccz .LBB0_2111
	s_barrier

.LBB0_2294:
	v_add_u32_e32 v79, s65, v167
	ds_read_b128 v[142:145], v79
	ds_read_b128 v[156:159], v79 offset:1024
	ds_read_b128 v[178:181], v79 offset:2048
	ds_read_b128 v[182:185], v79 offset:3072
	v_add_u32_e32 v79, s66, v167
	ds_read_b128 v[186:189], v79
	ds_read_b128 v[190:193], v79 offset:1024
	ds_read_b128 v[196:199], v79 offset:2048
	ds_read_b128 v[200:203], v79 offset:3072
	s_add_u32 s40, s8, 0x100
	s_addc_u32 s41, s9, 0
	s_cmpk_eq_i32 s8, 0x700
	s_cselect_b64 vcc, -1, 0
	v_lshl_add_u64 v[160:161], v[88:89], 0, s[8:9]
	s_and_b64 s[76:77], vcc, exec
	v_cndmask_b32_e32 v161, v161, v155, vcc
	s_cselect_b32 s75, 0, s40
	v_cndmask_b32_e32 v160, v160, v154, vcc
	v_lshl_add_u64 v[236:237], v[140:141], 0, s[8:9]
	s_add_i32 m0, s42, 0xc000
	ds_read_b128 v[204:207], v169
	ds_read_b128 v[208:211], v169 offset:1024
	ds_read_b128 v[212:215], v169 offset:2048
	ds_read_b128 v[216:219], v169 offset:3072
	ds_read_b128 v[220:223], v169 offset:4096
	ds_read_b128 v[224:227], v169 offset:5120
	ds_read_b128 v[228:231], v169 offset:6144
	ds_read_b128 v[232:235], v169 offset:7168
	global_load_lds_dwordx4 v[236:237], off
	v_lshl_add_u64 v[236:237], v[138:139], 0, s[8:9]
	s_add_i32 m0, s42, 0xe000
	s_nop 0
	global_load_lds_dwordx4 v[236:237], off
	s_waitcnt vmcnt(8)
	s_waitcnt lgkmcnt(0)
	s_barrier
	s_setprio 1
	s_waitcnt lgkmcnt(0)
	v_mfma_i32_16x16x64_i8 v[134:137], v[142:145], v[204:207], v[134:137]
	v_mfma_i32_16x16x64_i8 v[126:129], v[178:181], v[204:207], v[126:129]
	v_mfma_i32_16x16x64_i8 v[118:121], v[142:145], v[212:215], v[118:121]
	v_mfma_i32_16x16x64_i8 v[110:113], v[178:181], v[212:215], v[110:113]
	v_mfma_i32_16x16x64_i8 v[102:105], v[142:145], v[220:223], v[102:105]
	v_mfma_i32_16x16x64_i8 v[94:97], v[178:181], v[220:223], v[94:97]
	v_mfma_i32_16x16x64_i8 v[82:85], v[142:145], v[228:231], v[82:85]
	v_mfma_i32_16x16x64_i8 v[70:73], v[178:181], v[228:231], v[70:73]
	v_mfma_i32_16x16x64_i8 v[134:137], v[156:159], v[208:211], v[134:137]
	v_mfma_i32_16x16x64_i8 v[126:129], v[182:185], v[208:211], v[126:129]
	v_mfma_i32_16x16x64_i8 v[118:121], v[156:159], v[216:219], v[118:121]
	v_mfma_i32_16x16x64_i8 v[110:113], v[182:185], v[216:219], v[110:113]
	v_mfma_i32_16x16x64_i8 v[102:105], v[156:159], v[224:227], v[102:105]
	v_mfma_i32_16x16x64_i8 v[94:97], v[182:185], v[224:227], v[94:97]
	v_mfma_i32_16x16x64_i8 v[82:85], v[156:159], v[232:235], v[82:85]
	v_mfma_i32_16x16x64_i8 v[70:73], v[182:185], v[232:235], v[70:73]
	s_setprio 0
	s_setprio 1
	v_mfma_i32_16x16x64_i8 v[130:133], v[186:189], v[204:207], v[130:133]
	v_mfma_i32_16x16x64_i8 v[122:125], v[196:199], v[204:207], v[122:125]
	v_mfma_i32_16x16x64_i8 v[114:117], v[186:189], v[212:215], v[114:117]
	v_mfma_i32_16x16x64_i8 v[106:109], v[196:199], v[212:215], v[106:109]
	v_mfma_i32_16x16x64_i8 v[98:101], v[186:189], v[220:223], v[98:101]
	v_mfma_i32_16x16x64_i8 v[90:93], v[196:199], v[220:223], v[90:93]
	v_mfma_i32_16x16x64_i8 v[74:77], v[186:189], v[228:231], v[74:77]
	v_mfma_i32_16x16x64_i8 v[66:69], v[196:199], v[228:231], v[66:69]
	v_mfma_i32_16x16x64_i8 v[130:133], v[190:193], v[208:211], v[130:133]
	v_mfma_i32_16x16x64_i8 v[122:125], v[200:203], v[208:211], v[122:125]
	v_mfma_i32_16x16x64_i8 v[114:117], v[190:193], v[216:219], v[114:117]
	v_mfma_i32_16x16x64_i8 v[106:109], v[200:203], v[216:219], v[106:109]
	v_mfma_i32_16x16x64_i8 v[98:101], v[190:193], v[224:227], v[98:101]
	v_mfma_i32_16x16x64_i8 v[90:93], v[200:203], v[224:227], v[90:93]
	v_mfma_i32_16x16x64_i8 v[74:77], v[190:193], v[232:235], v[74:77]
	v_mfma_i32_16x16x64_i8 v[66:69], v[200:203], v[232:235], v[66:69]
	s_setprio 0
	s_add_i32 s8, s65, s33
	v_lshl_add_u64 v[236:237], v[160:161], 0, v[148:149]
	s_mov_b32 m0, s8
	s_barrier
	ds_read_b128 v[204:207], v169 offset:16384
	ds_read_b128 v[208:211], v169 offset:17408
	ds_read_b128 v[212:215], v169 offset:18432
	ds_read_b128 v[216:219], v169 offset:19456
	ds_read_b128 v[220:223], v169 offset:20480
	ds_read_b128 v[224:227], v169 offset:21504
	ds_read_b128 v[228:231], v169 offset:22528
	ds_read_b128 v[232:235], v169 offset:23552
	global_load_lds_dwordx4 v[236:237], off
	v_lshl_add_u64 v[238:239], v[160:161], 0, v[150:151]
	s_add_i32 m0, s8, 0x2000
	v_lshl_add_u64 v[240:241], v[160:161], 0, s[10:11]
	s_add_i32 s8, s66, s33
	global_load_lds_dwordx4 v[238:239], off
	v_lshl_add_u64 v[242:243], v[240:241], 0, v[148:149]
	s_mov_b32 m0, s8
	v_lshl_add_u64 v[240:241], v[240:241], 0, v[150:151]
	global_load_lds_dwordx4 v[242:243], off
	s_add_i32 m0, s8, 0x2000
	s_add_u32 s8, s60, s75
	global_load_lds_dwordx4 v[240:241], off
	v_cndmask_b32_e32 v146, v81, v173, vcc
	s_addc_u32 s9, s61, 0
	s_mov_b32 m0, s42
	v_cndmask_b32_e32 v240, v80, v174, vcc
	global_load_lds_dwordx4 v146, s[8:9]
	s_mov_b32 m0, s43
	v_mov_b32_e32 v241, v147
	global_load_lds_dwordx4 v240, s[8:9]
	s_waitcnt vmcnt(8)
	s_waitcnt lgkmcnt(0)
	v_lshl_add_u64 v[242:243], s[8:9], 0, v[146:147]
	v_lshl_add_u64 v[240:241], s[8:9], 0, v[240:241]
	s_barrier
	s_setprio 1
	s_waitcnt lgkmcnt(0)
	v_mfma_i32_16x16x64_i8 v[54:57], v[142:145], v[204:207], v[54:57]
	v_mfma_i32_16x16x64_i8 v[50:53], v[178:181], v[204:207], v[50:53]
	v_mfma_i32_16x16x64_i8 v[42:45], v[142:145], v[212:215], v[42:45]
	v_mfma_i32_16x16x64_i8 v[34:37], v[178:181], v[212:215], v[34:37]
	v_mfma_i32_16x16x64_i8 v[26:29], v[142:145], v[220:223], v[26:29]
	v_mfma_i32_16x16x64_i8 v[18:21], v[178:181], v[220:223], v[18:21]
	v_mfma_i32_16x16x64_i8 v[10:13], v[142:145], v[228:231], v[10:13]
	v_mfma_i32_16x16x64_i8 v[2:5], v[178:181], v[228:231], v[2:5]
	v_mfma_i32_16x16x64_i8 v[54:57], v[156:159], v[208:211], v[54:57]
	v_mfma_i32_16x16x64_i8 v[50:53], v[182:185], v[208:211], v[50:53]
	v_mfma_i32_16x16x64_i8 v[42:45], v[156:159], v[216:219], v[42:45]
	v_mfma_i32_16x16x64_i8 v[34:37], v[182:185], v[216:219], v[34:37]
	v_mfma_i32_16x16x64_i8 v[26:29], v[156:159], v[224:227], v[26:29]
	v_mfma_i32_16x16x64_i8 v[18:21], v[182:185], v[224:227], v[18:21]
	v_mfma_i32_16x16x64_i8 v[10:13], v[156:159], v[232:235], v[10:13]
	v_mfma_i32_16x16x64_i8 v[2:5], v[182:185], v[232:235], v[2:5]
	s_setprio 0
	s_setprio 1
	v_mfma_i32_16x16x64_i8 v[62:65], v[186:189], v[204:207], v[62:65]
	v_mfma_i32_16x16x64_i8 v[58:61], v[196:199], v[204:207], v[58:61]
	v_mfma_i32_16x16x64_i8 v[46:49], v[186:189], v[212:215], v[46:49]
	v_mfma_i32_16x16x64_i8 v[38:41], v[196:199], v[212:215], v[38:41]
	v_mfma_i32_16x16x64_i8 v[30:33], v[186:189], v[220:223], v[30:33]
	v_mfma_i32_16x16x64_i8 v[22:25], v[196:199], v[220:223], v[22:25]
	v_mfma_i32_16x16x64_i8 v[14:17], v[186:189], v[228:231], v[14:17]
	v_mfma_i32_16x16x64_i8 v[6:9], v[196:199], v[228:231], v[6:9]
	v_mfma_i32_16x16x64_i8 v[62:65], v[190:193], v[208:211], v[62:65]
	v_mfma_i32_16x16x64_i8 v[58:61], v[200:203], v[208:211], v[58:61]
	v_mfma_i32_16x16x64_i8 v[46:49], v[190:193], v[216:219], v[46:49]
	v_mfma_i32_16x16x64_i8 v[38:41], v[200:203], v[216:219], v[38:41]
	v_mfma_i32_16x16x64_i8 v[30:33], v[190:193], v[224:227], v[30:33]
	v_mfma_i32_16x16x64_i8 v[22:25], v[200:203], v[224:227], v[22:25]
	v_mfma_i32_16x16x64_i8 v[14:17], v[190:193], v[232:235], v[14:17]
	v_mfma_i32_16x16x64_i8 v[6:9], v[200:203], v[232:235], v[6:9]
	s_setprio 0
	s_add_i32 s75, 0, 0x18000
	v_add_u32_e32 v79, s75, v167
	s_add_i32 s76, 0, 0x1c000
	s_barrier
	ds_read_b128 v[142:145], v79
	ds_read_b128 v[156:159], v79 offset:1024
	ds_read_b128 v[178:181], v79 offset:2048
	ds_read_b128 v[182:185], v79 offset:3072
	v_add_u32_e32 v79, s76, v167
	ds_read_b128 v[186:189], v79
	ds_read_b128 v[190:193], v79 offset:1024
	ds_read_b128 v[196:199], v79 offset:2048
	ds_read_b128 v[200:203], v79 offset:3072
	s_mov_b32 m0, s44
	v_cndmask_b32_e32 v79, v78, v175, vcc
	ds_read_b128 v[204:207], v169 offset:32768
	ds_read_b128 v[208:211], v169 offset:33792
	ds_read_b128 v[212:215], v169 offset:34816
	ds_read_b128 v[216:219], v169 offset:35840
	ds_read_b128 v[220:223], v169 offset:36864
	ds_read_b128 v[224:227], v169 offset:37888
	ds_read_b128 v[228:231], v169 offset:38912
	ds_read_b128 v[232:235], v169 offset:39936
	v_cndmask_b32_e32 v87, v86, v176, vcc
	global_load_lds_dwordx4 v79, s[8:9]
	s_mov_b32 m0, s45
	s_nop 0
	global_load_lds_dwordx4 v87, s[8:9]
	s_waitcnt vmcnt(8)
	s_waitcnt lgkmcnt(0)
	s_barrier
	s_setprio 1
	s_waitcnt lgkmcnt(0)
	v_mfma_i32_16x16x64_i8 v[134:137], v[142:145], v[204:207], v[134:137]
	v_mfma_i32_16x16x64_i8 v[126:129], v[178:181], v[204:207], v[126:129]
	v_mfma_i32_16x16x64_i8 v[118:121], v[142:145], v[212:215], v[118:121]
	v_mfma_i32_16x16x64_i8 v[110:113], v[178:181], v[212:215], v[110:113]
	v_mfma_i32_16x16x64_i8 v[102:105], v[142:145], v[220:223], v[102:105]
	v_mfma_i32_16x16x64_i8 v[94:97], v[178:181], v[220:223], v[94:97]
	v_mfma_i32_16x16x64_i8 v[82:85], v[142:145], v[228:231], v[82:85]
	v_mfma_i32_16x16x64_i8 v[70:73], v[178:181], v[228:231], v[70:73]
	v_mfma_i32_16x16x64_i8 v[134:137], v[156:159], v[208:211], v[134:137]
	v_mfma_i32_16x16x64_i8 v[126:129], v[182:185], v[208:211], v[126:129]
	v_mfma_i32_16x16x64_i8 v[118:121], v[156:159], v[216:219], v[118:121]
	v_mfma_i32_16x16x64_i8 v[110:113], v[182:185], v[216:219], v[110:113]
	v_mfma_i32_16x16x64_i8 v[102:105], v[156:159], v[224:227], v[102:105]
	v_mfma_i32_16x16x64_i8 v[94:97], v[182:185], v[224:227], v[94:97]
	v_mfma_i32_16x16x64_i8 v[82:85], v[156:159], v[232:235], v[82:85]
	v_mfma_i32_16x16x64_i8 v[70:73], v[182:185], v[232:235], v[70:73]
	s_setprio 0
	s_setprio 1
	v_mfma_i32_16x16x64_i8 v[130:133], v[186:189], v[204:207], v[130:133]
	v_mfma_i32_16x16x64_i8 v[122:125], v[196:199], v[204:207], v[122:125]
	v_mfma_i32_16x16x64_i8 v[114:117], v[186:189], v[212:215], v[114:117]
	v_mfma_i32_16x16x64_i8 v[106:109], v[196:199], v[212:215], v[106:109]
	v_mfma_i32_16x16x64_i8 v[98:101], v[186:189], v[220:223], v[98:101]
	v_mfma_i32_16x16x64_i8 v[90:93], v[196:199], v[220:223], v[90:93]
	v_mfma_i32_16x16x64_i8 v[74:77], v[186:189], v[228:231], v[74:77]
	v_mfma_i32_16x16x64_i8 v[66:69], v[196:199], v[228:231], v[66:69]
	v_mfma_i32_16x16x64_i8 v[130:133], v[190:193], v[208:211], v[130:133]
	v_mfma_i32_16x16x64_i8 v[122:125], v[200:203], v[208:211], v[122:125]
	v_mfma_i32_16x16x64_i8 v[114:117], v[190:193], v[216:219], v[114:117]
	v_mfma_i32_16x16x64_i8 v[106:109], v[200:203], v[216:219], v[106:109]
	v_mfma_i32_16x16x64_i8 v[98:101], v[190:193], v[224:227], v[98:101]
	v_mfma_i32_16x16x64_i8 v[90:93], v[200:203], v[224:227], v[90:93]
	v_mfma_i32_16x16x64_i8 v[74:77], v[190:193], v[232:235], v[74:77]
	v_mfma_i32_16x16x64_i8 v[66:69], v[200:203], v[232:235], v[66:69]
	s_setprio 0
	s_add_i32 s8, s75, s33
	v_lshl_add_u64 v[236:237], v[236:237], 0, s[20:21]
	s_mov_b32 m0, s8
	s_barrier
	ds_read_b128 v[204:207], v169 offset:49152
	ds_read_b128 v[208:211], v169 offset:50176
	ds_read_b128 v[212:215], v169 offset:51200
	ds_read_b128 v[216:219], v169 offset:52224
	ds_read_b128 v[220:223], v169 offset:53248
	ds_read_b128 v[224:227], v169 offset:54272
	ds_read_b128 v[228:231], v169 offset:55296
	ds_read_b128 v[232:235], v169 offset:56320
	global_load_lds_dwordx4 v[236:237], off
	v_lshl_add_u64 v[236:237], v[238:239], 0, s[20:21]
	s_add_i32 m0, s8, 0x2000
	v_lshl_add_u64 v[160:161], v[160:161], 0, s[24:25]
	s_add_i32 s8, s76, s33
	global_load_lds_dwordx4 v[236:237], off
	v_lshl_add_u64 v[236:237], v[160:161], 0, v[148:149]
	s_mov_b32 m0, s8
	v_lshl_add_u64 v[160:161], v[160:161], 0, v[150:151]
	global_load_lds_dwordx4 v[236:237], off
	s_add_i32 m0, s8, 0x2000
	s_nop 0
	global_load_lds_dwordx4 v[160:161], off
	v_lshl_add_u64 v[160:161], v[242:243], 0, s[20:21]
	s_mov_b32 m0, s46
	s_nop 0
	global_load_lds_dwordx4 v[160:161], off
	v_lshl_add_u64 v[160:161], v[240:241], 0, s[20:21]
	s_mov_b32 m0, s47
	s_nop 0
	global_load_lds_dwordx4 v[160:161], off
	s_waitcnt vmcnt(8)
	s_waitcnt lgkmcnt(0)
	s_barrier
	s_setprio 1
	s_waitcnt lgkmcnt(0)
	v_mfma_i32_16x16x64_i8 v[54:57], v[142:145], v[204:207], v[54:57]
	v_mfma_i32_16x16x64_i8 v[50:53], v[178:181], v[204:207], v[50:53]
	v_mfma_i32_16x16x64_i8 v[42:45], v[142:145], v[212:215], v[42:45]
	v_mfma_i32_16x16x64_i8 v[34:37], v[178:181], v[212:215], v[34:37]
	v_mfma_i32_16x16x64_i8 v[26:29], v[142:145], v[220:223], v[26:29]
	v_mfma_i32_16x16x64_i8 v[18:21], v[178:181], v[220:223], v[18:21]
	v_mfma_i32_16x16x64_i8 v[10:13], v[142:145], v[228:231], v[10:13]
	v_mfma_i32_16x16x64_i8 v[2:5], v[178:181], v[228:231], v[2:5]
	v_mfma_i32_16x16x64_i8 v[54:57], v[156:159], v[208:211], v[54:57]
	v_mfma_i32_16x16x64_i8 v[50:53], v[182:185], v[208:211], v[50:53]
	v_mfma_i32_16x16x64_i8 v[42:45], v[156:159], v[216:219], v[42:45]
	v_mfma_i32_16x16x64_i8 v[34:37], v[182:185], v[216:219], v[34:37]
	v_mfma_i32_16x16x64_i8 v[26:29], v[156:159], v[224:227], v[26:29]
	v_mfma_i32_16x16x64_i8 v[18:21], v[182:185], v[224:227], v[18:21]
	v_mfma_i32_16x16x64_i8 v[10:13], v[156:159], v[232:235], v[10:13]
	v_mfma_i32_16x16x64_i8 v[2:5], v[182:185], v[232:235], v[2:5]
	s_setprio 0
	s_setprio 1
	v_mfma_i32_16x16x64_i8 v[62:65], v[186:189], v[204:207], v[62:65]
	v_mfma_i32_16x16x64_i8 v[58:61], v[196:199], v[204:207], v[58:61]
	v_mfma_i32_16x16x64_i8 v[46:49], v[186:189], v[212:215], v[46:49]
	v_mfma_i32_16x16x64_i8 v[38:41], v[196:199], v[212:215], v[38:41]
	v_mfma_i32_16x16x64_i8 v[30:33], v[186:189], v[220:223], v[30:33]
	v_mfma_i32_16x16x64_i8 v[22:25], v[196:199], v[220:223], v[22:25]
	v_mfma_i32_16x16x64_i8 v[14:17], v[186:189], v[228:231], v[14:17]
	v_mfma_i32_16x16x64_i8 v[6:9], v[196:199], v[228:231], v[6:9]
	v_mfma_i32_16x16x64_i8 v[62:65], v[190:193], v[208:211], v[62:65]
	v_mfma_i32_16x16x64_i8 v[58:61], v[200:203], v[208:211], v[58:61]
	v_mfma_i32_16x16x64_i8 v[46:49], v[190:193], v[216:219], v[46:49]
	v_mfma_i32_16x16x64_i8 v[38:41], v[200:203], v[216:219], v[38:41]
	v_mfma_i32_16x16x64_i8 v[30:33], v[190:193], v[224:227], v[30:33]
	v_mfma_i32_16x16x64_i8 v[22:25], v[200:203], v[224:227], v[22:25]
	v_mfma_i32_16x16x64_i8 v[14:17], v[190:193], v[232:235], v[14:17]
	v_mfma_i32_16x16x64_i8 v[6:9], v[200:203], v[232:235], v[6:9]
	s_setprio 0
	s_add_i32 s37, s37, 2
	s_cmp_gt_u32 s37, 13
	s_mov_b64 s[8:9], s[40:41]
	s_barrier
	s_cbranch_scc0 .LBB0_2294
	s_and_b64 vcc, exec, s[26:27]
	s_cbranch_vccz .LBB0_2297
	s_barrier

.LBB0_2387:
	ds_read_b128 v[18:21], v198
	ds_read_b128 v[22:25], v198 offset:1024
	ds_read_b128 v[26:29], v198 offset:2048
	ds_read_b128 v[30:33], v198 offset:3072
	ds_read_b128 v[2:5], v199
	ds_read_b128 v[6:9], v199 offset:1024
	ds_read_b128 v[10:13], v199 offset:2048
	ds_read_b128 v[14:17], v199 offset:3072
	s_add_u32 s42, s44, 0x100
	s_addc_u32 s43, s45, 0
	s_add_i32 s76, s63, s4
	s_add_i32 m0, s33, 0xc000
	s_add_i32 s77, s33, 0xe000
	s_add_i32 s74, s76, 0x2000
	s_cmp_eq_u32 s71, 18
	v_lshl_add_u64 v[184:185], v[178:179], 0, s[44:45]
	s_cselect_b64 vcc, -1, 0
	s_cselect_b32 s75, 0, s42
	v_cndmask_b32_e32 v185, v185, v177, vcc
	v_cndmask_b32_e32 v184, v184, v176, vcc
	v_lshl_add_u64 v[226:227], v[180:181], 0, s[44:45]
	ds_read_b128 v[186:189], v200
	ds_read_b128 v[190:193], v200 offset:1024
	ds_read_b128 v[202:205], v200 offset:2048
	ds_read_b128 v[206:209], v200 offset:3072
	ds_read_b128 v[210:213], v200 offset:4096
	ds_read_b128 v[214:217], v200 offset:5120
	ds_read_b128 v[218:221], v200 offset:6144
	ds_read_b128 v[222:225], v200 offset:7168
	global_load_lds_dwordx4 v[226:227], off
	v_lshl_add_u64 v[226:227], v[182:183], 0, s[44:45]
	s_mov_b32 m0, s77
	s_nop 0
	global_load_lds_dwordx4 v[226:227], off
	s_waitcnt vmcnt(8)
	s_waitcnt lgkmcnt(0)
	s_barrier
	s_setprio 1
	s_waitcnt lgkmcnt(0)
	v_mfma_scale_f32_16x16x128_f8f6f4 v[158:161], v[18:25], v[186:193], v[158:161], v1, v1 op_sel_hi:[0,0,0]
	v_mfma_scale_f32_16x16x128_f8f6f4 v[154:157], v[26:33], v[186:193], v[154:157], v1, v1 op_sel_hi:[0,0,0]
	v_mfma_scale_f32_16x16x128_f8f6f4 v[150:153], v[18:25], v[202:209], v[150:153], v1, v1 op_sel_hi:[0,0,0]
	v_mfma_scale_f32_16x16x128_f8f6f4 v[142:145], v[26:33], v[202:209], v[142:145], v1, v1 op_sel_hi:[0,0,0]
	v_mfma_scale_f32_16x16x128_f8f6f4 v[134:137], v[18:25], v[210:217], v[134:137], v1, v1 op_sel_hi:[0,0,0]
	v_mfma_scale_f32_16x16x128_f8f6f4 v[126:129], v[26:33], v[210:217], v[126:129], v1, v1 op_sel_hi:[0,0,0]
	v_mfma_scale_f32_16x16x128_f8f6f4 v[118:121], v[18:25], v[218:225], v[118:121], v1, v1 op_sel_hi:[0,0,0]
	v_mfma_scale_f32_16x16x128_f8f6f4 v[110:113], v[26:33], v[218:225], v[110:113], v1, v1 op_sel_hi:[0,0,0]
	s_setprio 0
	s_setprio 1
	v_mfma_scale_f32_16x16x128_f8f6f4 v[146:149], v[2:9], v[186:193], v[146:149], v1, v1 op_sel_hi:[0,0,0]
	v_mfma_scale_f32_16x16x128_f8f6f4 v[138:141], v[10:17], v[186:193], v[138:141], v1, v1 op_sel_hi:[0,0,0]
	v_mfma_scale_f32_16x16x128_f8f6f4 v[130:133], v[2:9], v[202:209], v[130:133], v1, v1 op_sel_hi:[0,0,0]
	v_mfma_scale_f32_16x16x128_f8f6f4 v[122:125], v[10:17], v[202:209], v[122:125], v1, v1 op_sel_hi:[0,0,0]
	v_mfma_scale_f32_16x16x128_f8f6f4 v[114:117], v[2:9], v[210:217], v[114:117], v1, v1 op_sel_hi:[0,0,0]
	v_mfma_scale_f32_16x16x128_f8f6f4 v[106:109], v[10:17], v[210:217], v[106:109], v1, v1 op_sel_hi:[0,0,0]
	v_mfma_scale_f32_16x16x128_f8f6f4 v[102:105], v[2:9], v[218:225], v[102:105], v1, v1 op_sel_hi:[0,0,0]
	v_mfma_scale_f32_16x16x128_f8f6f4 v[98:101], v[10:17], v[218:225], v[98:101], v1, v1 op_sel_hi:[0,0,0]
	s_setprio 0
	s_mov_b32 m0, s76
	v_lshl_add_u64 v[188:189], v[184:185], 0, v[170:171]
	s_barrier
	ds_read_b128 v[202:205], v200 offset:16384
	ds_read_b128 v[206:209], v200 offset:17408
	ds_read_b128 v[210:213], v200 offset:18432
	ds_read_b128 v[214:217], v200 offset:19456
	ds_read_b128 v[218:221], v200 offset:20480
	ds_read_b128 v[222:225], v200 offset:21504
	ds_read_b128 v[226:229], v200 offset:22528
	ds_read_b128 v[230:233], v200 offset:23552
	global_load_lds_dwordx4 v[188:189], off
	v_lshl_add_u64 v[186:187], v[184:185], 0, v[164:165]
	s_mov_b32 m0, s74
	s_cselect_b32 s45, s9, s41
	s_cselect_b32 s44, s8, s40
	v_lshl_add_u64 v[190:191], v[184:185], 0, s[12:13]
	s_add_i32 s74, s64, s4
	global_load_lds_dwordx4 v[186:187], off
	v_lshl_add_u64 v[192:193], v[190:191], 0, v[170:171]
	s_mov_b32 m0, s74
	v_lshl_add_u64 v[190:191], v[190:191], 0, v[164:165]
	global_load_lds_dwordx4 v[192:193], off
	s_add_i32 m0, s74, 0x2000
	s_add_u32 s44, s44, s75
	s_addc_u32 s45, s45, 0
	global_load_lds_dwordx4 v[190:191], off
	v_lshl_add_u64 v[190:191], s[44:45], 0, v[166:167]
	s_mov_b32 m0, s33
	v_lshl_add_u64 v[192:193], s[44:45], 0, v[168:169]
	global_load_lds_dwordx4 v[190:191], off
	s_mov_b32 m0, s39
	s_nop 0
	global_load_lds_dwordx4 v[192:193], off
	s_waitcnt vmcnt(8)
	s_waitcnt lgkmcnt(0)
	s_barrier
	s_setprio 1
	s_waitcnt lgkmcnt(0)
	v_mfma_scale_f32_16x16x128_f8f6f4 v[94:97], v[18:25], v[202:209], v[94:97], v1, v1 op_sel_hi:[0,0,0]
	v_mfma_scale_f32_16x16x128_f8f6f4 v[90:93], v[26:33], v[202:209], v[90:93], v1, v1 op_sel_hi:[0,0,0]
	v_mfma_scale_f32_16x16x128_f8f6f4 v[86:89], v[18:25], v[210:217], v[86:89], v1, v1 op_sel_hi:[0,0,0]
	v_mfma_scale_f32_16x16x128_f8f6f4 v[78:81], v[26:33], v[210:217], v[78:81], v1, v1 op_sel_hi:[0,0,0]
	v_mfma_scale_f32_16x16x128_f8f6f4 v[62:65], v[18:25], v[218:225], v[62:65], v1, v1 op_sel_hi:[0,0,0]
	v_mfma_scale_f32_16x16x128_f8f6f4 v[54:57], v[26:33], v[218:225], v[54:57], v1, v1 op_sel_hi:[0,0,0]
	v_mfma_scale_f32_16x16x128_f8f6f4 v[46:49], v[18:25], v[226:233], v[46:49], v1, v1 op_sel_hi:[0,0,0]
	v_mfma_scale_f32_16x16x128_f8f6f4 v[38:41], v[26:33], v[226:233], v[38:41], v1, v1 op_sel_hi:[0,0,0]
	s_setprio 0
	s_setprio 1
	v_mfma_scale_f32_16x16x128_f8f6f4 v[82:85], v[2:9], v[202:209], v[82:85], v1, v1 op_sel_hi:[0,0,0]
	v_mfma_scale_f32_16x16x128_f8f6f4 v[74:77], v[10:17], v[202:209], v[74:77], v1, v1 op_sel_hi:[0,0,0]
	v_mfma_scale_f32_16x16x128_f8f6f4 v[58:61], v[2:9], v[210:217], v[58:61], v1, v1 op_sel_hi:[0,0,0]
	v_mfma_scale_f32_16x16x128_f8f6f4 v[50:53], v[10:17], v[210:217], v[50:53], v1, v1 op_sel_hi:[0,0,0]
	v_mfma_scale_f32_16x16x128_f8f6f4 v[42:45], v[2:9], v[218:225], v[42:45], v1, v1 op_sel_hi:[0,0,0]
	v_mfma_scale_f32_16x16x128_f8f6f4 v[34:37], v[10:17], v[218:225], v[34:37], v1, v1 op_sel_hi:[0,0,0]
	v_mfma_scale_f32_16x16x128_f8f6f4 v[70:73], v[2:9], v[226:233], v[70:73], v1, v1 op_sel_hi:[0,0,0]
	v_mfma_scale_f32_16x16x128_f8f6f4 v[66:69], v[10:17], v[226:233], v[66:69], v1, v1 op_sel_hi:[0,0,0]
	s_setprio 0
	s_add_i32 s74, 0, 0x18000
	s_add_i32 s75, 0, 0x1c000
	v_add_u32_e32 v14, s74, v196
	v_add_u32_e32 v30, s75, v196
	s_barrier
	ds_read_b128 v[2:5], v14
	ds_read_b128 v[6:9], v14 offset:1024
	ds_read_b128 v[10:13], v14 offset:2048
	ds_read_b128 v[14:17], v14 offset:3072
	ds_read_b128 v[18:21], v30
	ds_read_b128 v[22:25], v30 offset:1024
	ds_read_b128 v[26:29], v30 offset:2048
	ds_read_b128 v[30:33], v30 offset:3072
	s_add_u32 s44, s44, 0x58000
	s_addc_u32 s45, s45, 0
	s_mov_b32 m0, s46
	v_lshl_add_u64 v[234:235], s[44:45], 0, v[166:167]
	ds_read_b128 v[202:205], v200 offset:32768
	ds_read_b128 v[206:209], v200 offset:33792
	ds_read_b128 v[210:213], v200 offset:34816
	ds_read_b128 v[214:217], v200 offset:35840
	ds_read_b128 v[218:221], v200 offset:36864
	ds_read_b128 v[222:225], v200 offset:37888
	ds_read_b128 v[226:229], v200 offset:38912
	ds_read_b128 v[230:233], v200 offset:39936
	global_load_lds_dwordx4 v[234:235], off
	v_lshl_add_u64 v[234:235], s[44:45], 0, v[168:169]
	s_mov_b32 m0, s47
	s_nop 0
	global_load_lds_dwordx4 v[234:235], off
	s_waitcnt vmcnt(8)
	s_waitcnt lgkmcnt(0)
	s_barrier
	s_setprio 1
	s_waitcnt lgkmcnt(0)
	v_mfma_scale_f32_16x16x128_f8f6f4 v[158:161], v[2:9], v[202:209], v[158:161], v1, v1 op_sel_hi:[0,0,0]
	v_mfma_scale_f32_16x16x128_f8f6f4 v[154:157], v[10:17], v[202:209], v[154:157], v1, v1 op_sel_hi:[0,0,0]
	v_mfma_scale_f32_16x16x128_f8f6f4 v[150:153], v[2:9], v[210:217], v[150:153], v1, v1 op_sel_hi:[0,0,0]
	v_mfma_scale_f32_16x16x128_f8f6f4 v[142:145], v[10:17], v[210:217], v[142:145], v1, v1 op_sel_hi:[0,0,0]
	v_mfma_scale_f32_16x16x128_f8f6f4 v[134:137], v[2:9], v[218:225], v[134:137], v1, v1 op_sel_hi:[0,0,0]
	v_mfma_scale_f32_16x16x128_f8f6f4 v[126:129], v[10:17], v[218:225], v[126:129], v1, v1 op_sel_hi:[0,0,0]
	v_mfma_scale_f32_16x16x128_f8f6f4 v[118:121], v[2:9], v[226:233], v[118:121], v1, v1 op_sel_hi:[0,0,0]
	v_mfma_scale_f32_16x16x128_f8f6f4 v[110:113], v[10:17], v[226:233], v[110:113], v1, v1 op_sel_hi:[0,0,0]
	s_setprio 0
	s_setprio 1
	v_mfma_scale_f32_16x16x128_f8f6f4 v[146:149], v[18:25], v[202:209], v[146:149], v1, v1 op_sel_hi:[0,0,0]
	v_mfma_scale_f32_16x16x128_f8f6f4 v[138:141], v[26:33], v[202:209], v[138:141], v1, v1 op_sel_hi:[0,0,0]
	v_mfma_scale_f32_16x16x128_f8f6f4 v[130:133], v[18:25], v[210:217], v[130:133], v1, v1 op_sel_hi:[0,0,0]
	v_mfma_scale_f32_16x16x128_f8f6f4 v[122:125], v[26:33], v[210:217], v[122:125], v1, v1 op_sel_hi:[0,0,0]
	v_mfma_scale_f32_16x16x128_f8f6f4 v[114:117], v[18:25], v[218:225], v[114:117], v1, v1 op_sel_hi:[0,0,0]
	v_mfma_scale_f32_16x16x128_f8f6f4 v[106:109], v[26:33], v[218:225], v[106:109], v1, v1 op_sel_hi:[0,0,0]
	v_mfma_scale_f32_16x16x128_f8f6f4 v[102:105], v[18:25], v[226:233], v[102:105], v1, v1 op_sel_hi:[0,0,0]
	v_mfma_scale_f32_16x16x128_f8f6f4 v[98:101], v[26:33], v[226:233], v[98:101], v1, v1 op_sel_hi:[0,0,0]
	s_setprio 0
	s_add_i32 s44, s74, s4
	v_lshl_add_u64 v[188:189], v[188:189], 0, s[16:17]
	s_mov_b32 m0, s44
	s_barrier
	ds_read_b128 v[202:205], v200 offset:49152
	ds_read_b128 v[206:209], v200 offset:50176
	ds_read_b128 v[210:213], v200 offset:51200
	ds_read_b128 v[214:217], v200 offset:52224
	ds_read_b128 v[218:221], v200 offset:53248
	ds_read_b128 v[222:225], v200 offset:54272
	ds_read_b128 v[226:229], v200 offset:55296
	ds_read_b128 v[230:233], v200 offset:56320
	global_load_lds_dwordx4 v[188:189], off
	v_lshl_add_u64 v[186:187], v[186:187], 0, s[16:17]
	s_add_i32 m0, s44, 0x2000
	v_lshl_add_u64 v[184:185], v[184:185], 0, s[18:19]
	s_add_i32 s44, s75, s4
	global_load_lds_dwordx4 v[186:187], off
	v_lshl_add_u64 v[186:187], v[184:185], 0, v[170:171]
	s_mov_b32 m0, s44
	v_lshl_add_u64 v[184:185], v[184:185], 0, v[164:165]
	global_load_lds_dwordx4 v[186:187], off
	s_add_i32 m0, s44, 0x2000
	s_nop 0
	global_load_lds_dwordx4 v[184:185], off
	v_lshl_add_u64 v[184:185], v[190:191], 0, s[16:17]
	s_mov_b32 m0, s52
	s_nop 0
	global_load_lds_dwordx4 v[184:185], off
	v_lshl_add_u64 v[184:185], v[192:193], 0, s[16:17]
	s_mov_b32 m0, s53
	s_nop 0
	global_load_lds_dwordx4 v[184:185], off
	s_waitcnt vmcnt(8)
	s_waitcnt lgkmcnt(0)
	s_barrier
	s_setprio 1
	s_waitcnt lgkmcnt(0)
	v_mfma_scale_f32_16x16x128_f8f6f4 v[94:97], v[2:9], v[202:209], v[94:97], v1, v1 op_sel_hi:[0,0,0]
	v_mfma_scale_f32_16x16x128_f8f6f4 v[90:93], v[10:17], v[202:209], v[90:93], v1, v1 op_sel_hi:[0,0,0]
	v_mfma_scale_f32_16x16x128_f8f6f4 v[86:89], v[2:9], v[210:217], v[86:89], v1, v1 op_sel_hi:[0,0,0]
	v_mfma_scale_f32_16x16x128_f8f6f4 v[78:81], v[10:17], v[210:217], v[78:81], v1, v1 op_sel_hi:[0,0,0]
	v_mfma_scale_f32_16x16x128_f8f6f4 v[62:65], v[2:9], v[218:225], v[62:65], v1, v1 op_sel_hi:[0,0,0]
	v_mfma_scale_f32_16x16x128_f8f6f4 v[54:57], v[10:17], v[218:225], v[54:57], v1, v1 op_sel_hi:[0,0,0]
	v_mfma_scale_f32_16x16x128_f8f6f4 v[46:49], v[2:9], v[226:233], v[46:49], v1, v1 op_sel_hi:[0,0,0]
	v_mfma_scale_f32_16x16x128_f8f6f4 v[38:41], v[10:17], v[226:233], v[38:41], v1, v1 op_sel_hi:[0,0,0]
	s_setprio 0
	s_setprio 1
	v_mfma_scale_f32_16x16x128_f8f6f4 v[82:85], v[18:25], v[202:209], v[82:85], v1, v1 op_sel_hi:[0,0,0]
	v_mfma_scale_f32_16x16x128_f8f6f4 v[74:77], v[26:33], v[202:209], v[74:77], v1, v1 op_sel_hi:[0,0,0]
	v_mfma_scale_f32_16x16x128_f8f6f4 v[58:61], v[18:25], v[210:217], v[58:61], v1, v1 op_sel_hi:[0,0,0]
	v_mfma_scale_f32_16x16x128_f8f6f4 v[50:53], v[26:33], v[210:217], v[50:53], v1, v1 op_sel_hi:[0,0,0]
	v_mfma_scale_f32_16x16x128_f8f6f4 v[42:45], v[18:25], v[218:225], v[42:45], v1, v1 op_sel_hi:[0,0,0]
	v_mfma_scale_f32_16x16x128_f8f6f4 v[34:37], v[26:33], v[218:225], v[34:37], v1, v1 op_sel_hi:[0,0,0]
	v_mfma_scale_f32_16x16x128_f8f6f4 v[70:73], v[18:25], v[226:233], v[70:73], v1, v1 op_sel_hi:[0,0,0]
	v_mfma_scale_f32_16x16x128_f8f6f4 v[66:69], v[26:33], v[226:233], v[66:69], v1, v1 op_sel_hi:[0,0,0]
	s_setprio 0
	s_add_i32 s71, s71, 2
	s_cmp_gt_u32 s71, 19
	s_mov_b64 s[44:45], s[42:43]
	s_barrier
	s_cbranch_scc0 .LBB0_2387
	s_and_b64 vcc, exec, s[20:21]
	s_cbranch_vccz .LBB0_2390
	s_barrier
